# v43 + GQA attention: V tile staged with LDS image row = key, P^T fragments taken straight from the QK^T accumulators: no permlane32_swap per tile (fast path and fallback)
# speedup vs baseline: 1.0017x; 1.0017x over previous
.LBB0_873:
	v_exp_f32_e32 v101, v80
	v_exp_f32_e32 v103, v81
	v_exp_f32_e32 v111, v88
	v_exp_f32_e32 v89, v89
	v_exp_f32_e32 v105, v82
	v_exp_f32_e32 v113, v90
	v_exp_f32_e32 v83, v83
	v_exp_f32_e32 v91, v91
	v_exp_f32_e32 v107, v84
	v_exp_f32_e32 v115, v92
	v_mov_b32_e32 v100, v64
	v_mov_b32_e32 v102, v65
	v_mov_b32_e32 v110, v72
	v_mov_b32_e32 v88, v73
	v_exp_f32_e32 v85, v85
	v_exp_f32_e32 v93, v93
	v_pk_add_f32 v[80:81], v[100:101], v[102:103]
	v_pk_add_f32 v[118:119], v[110:111], v[88:89]
	v_mov_b32_e32 v104, v66
	v_mov_b32_e32 v112, v74
	v_exp_f32_e32 v109, v86
	v_exp_f32_e32 v117, v94
	v_pk_add_f32 v[80:81], v[104:105], v[80:81]
	v_pk_add_f32 v[118:119], v[112:113], v[118:119]
	v_mov_b32_e32 v82, v67
	v_mov_b32_e32 v90, v75
	v_exp_f32_e32 v87, v87
	v_exp_f32_e32 v95, v95
	v_pk_add_f32 v[80:81], v[82:83], v[80:81]
	v_pk_add_f32 v[118:119], v[90:91], v[118:119]
	v_mov_b32_e32 v106, v68
	v_mov_b32_e32 v114, v76
	v_pk_add_f32 v[80:81], v[106:107], v[80:81]
	v_pk_add_f32 v[118:119], v[114:115], v[118:119]
	v_mov_b32_e32 v84, v69
	v_mov_b32_e32 v92, v77
	v_pk_add_f32 v[80:81], v[84:85], v[80:81]
	v_pk_add_f32 v[118:119], v[92:93], v[118:119]
	v_mov_b32_e32 v108, v70
	v_mov_b32_e32 v116, v78
	v_pk_add_f32 v[80:81], v[108:109], v[80:81]
	v_pk_add_f32 v[118:119], v[116:117], v[118:119]
	v_mov_b32_e32 v86, v71
	v_mov_b32_e32 v94, v79
	v_pk_add_f32 v[80:81], v[86:87], v[80:81]
	v_pk_add_f32 v[118:119], v[94:95], v[118:119]
	s_lshl_b32 s2, s33, 12
	v_pk_add_f32 v[80:81], v[118:119], v[80:81]
	s_add_u32 s8, s35, s2
	v_pk_add_f32 v[80:81], v[80:81], v[80:81] op_sel:[0,1] op_sel_hi:[1,0]
	s_addc_u32 s9, s36, 0
	s_lshl_b32 s2, s28, 7
	v_mov_b32_e32 v99, v80
	s_ashr_i32 s3, s2, 31
	s_nop 0
	v_permlane32_swap_b32_e32 v80, v99
	s_lshl_b64 s[2:3], s[2:3], 1
	v_mul_f32_e32 v96, v217, v208
	v_add_f32_e32 v98, v142, v143
	v_mov_b32_e32 v97, v80
	s_add_u32 s8, s8, s2
	v_pk_add_f32 v[80:81], v[96:97], v[98:99]
	v_cvt_pk_bf16_f32 v64, v64, v65
	v_cvt_pk_bf16_f32 v65, v66, v67
	v_cvt_pk_bf16_f32 v66, v68, v69
	v_cvt_pk_bf16_f32 v67, v70, v71
	v_cvt_pk_bf16_f32 v68, v72, v73
	v_cvt_pk_bf16_f32 v69, v74, v75
	v_cvt_pk_bf16_f32 v70, v76, v77
	v_cvt_pk_bf16_f32 v71, v78, v79
	v_cvt_pk_bf16_f32 v72, v101, v103
	v_cvt_pk_bf16_f32 v73, v105, v83
	v_cvt_pk_bf16_f32 v74, v107, v85
	v_cvt_pk_bf16_f32 v75, v109, v87
	v_cvt_pk_bf16_f32 v76, v111, v89
	v_cvt_pk_bf16_f32 v77, v113, v91
	v_cvt_pk_bf16_f32 v78, v115, v93
	v_cvt_pk_bf16_f32 v79, v117, v95
	s_addc_u32 s9, s9, s3
	v_fmac_f32_e32 v81, v80, v128
	ds_read_b64_tr_b16 v[82:83], v211 offset:0
	ds_read_b64_tr_b16 v[84:85], v211 offset:0x800
	ds_read_b64_tr_b16 v[86:87], v211 offset:0x1000
	ds_read_b64_tr_b16 v[88:89], v211 offset:0x1800
	ds_read_b64_tr_b16 v[90:91], v211 offset:0x2000
	ds_read_b64_tr_b16 v[92:93], v211 offset:0x2800
	ds_read_b64_tr_b16 v[94:95], v211 offset:0x3000
	ds_read_b64_tr_b16 v[96:97], v211 offset:0x3800
	s_waitcnt lgkmcnt(0)
	s_nop 0
	v_mfma_f32_32x32x16_bf16 v[0:15], v[82:85], v[64:67], v[0:15]
	ds_read_b64_tr_b16 v[82:83], v211 offset:0x200
	ds_read_b64_tr_b16 v[84:85], v211 offset:0xa00
	v_mfma_f32_32x32x16_bf16 v[0:15], v[86:89], v[68:71], v[0:15]
	ds_read_b64_tr_b16 v[86:87], v211 offset:0x1200
	ds_read_b64_tr_b16 v[88:89], v211 offset:0x1a00
	v_mfma_f32_32x32x16_bf16 v[0:15], v[90:93], v[72:75], v[0:15]
	ds_read_b64_tr_b16 v[90:91], v211 offset:0x2200
	ds_read_b64_tr_b16 v[92:93], v211 offset:0x2a00
	v_mfma_f32_32x32x16_bf16 v[0:15], v[94:97], v[76:79], v[0:15]
	ds_read_b64_tr_b16 v[94:95], v211 offset:0x3200
	ds_read_b64_tr_b16 v[96:97], v211 offset:0x3a00
	s_waitcnt lgkmcnt(0)
	v_mfma_f32_32x32x16_bf16 v[48:63], v[82:85], v[64:67], v[48:63]
	ds_read_b64_tr_b16 v[82:83], v211 offset:0x400
	ds_read_b64_tr_b16 v[84:85], v211 offset:0xc00
	v_mfma_f32_32x32x16_bf16 v[48:63], v[86:89], v[68:71], v[48:63]
	ds_read_b64_tr_b16 v[86:87], v211 offset:0x1400
	ds_read_b64_tr_b16 v[88:89], v211 offset:0x1c00
	v_mfma_f32_32x32x16_bf16 v[48:63], v[90:93], v[72:75], v[48:63]
	ds_read_b64_tr_b16 v[90:91], v211 offset:0x2400
	ds_read_b64_tr_b16 v[92:93], v211 offset:0x2c00
	v_mfma_f32_32x32x16_bf16 v[48:63], v[94:97], v[76:79], v[48:63]
	ds_read_b64_tr_b16 v[94:95], v211 offset:0x3400
	ds_read_b64_tr_b16 v[96:97], v211 offset:0x3c00
	s_waitcnt lgkmcnt(0)
	v_mfma_f32_32x32x16_bf16 v[32:47], v[82:85], v[64:67], v[32:47]
	ds_read_b64_tr_b16 v[82:83], v211 offset:0x600
	ds_read_b64_tr_b16 v[84:85], v211 offset:0xe00
	v_mfma_f32_32x32x16_bf16 v[32:47], v[86:89], v[68:71], v[32:47]
	ds_read_b64_tr_b16 v[86:87], v211 offset:0x1600
	ds_read_b64_tr_b16 v[88:89], v211 offset:0x1e00
	v_mfma_f32_32x32x16_bf16 v[32:47], v[90:93], v[72:75], v[32:47]
	ds_read_b64_tr_b16 v[90:91], v211 offset:0x2600
	ds_read_b64_tr_b16 v[92:93], v211 offset:0x2e00
	v_mfma_f32_32x32x16_bf16 v[32:47], v[94:97], v[76:79], v[32:47]
	ds_read_b64_tr_b16 v[94:95], v211 offset:0x3600
	ds_read_b64_tr_b16 v[96:97], v211 offset:0x3e00
	s_waitcnt lgkmcnt(0)
	v_mfma_f32_32x32x16_bf16 v[16:31], v[82:85], v[64:67], v[16:31]
	v_rcp_f32_e32 v67, v81
	v_mbcnt_lo_u32_b32 v66, -1, 0
	v_mbcnt_hi_u32_b32 v66, -1, v66
	s_add_i32 s20, s20, 1
	v_add_u32_e32 v64, s80, v66
	v_ashrrev_i32_e32 v64, 1, v64
	v_mul_f32_e32 v0, v67, v0
	v_mul_f32_e32 v1, v67, v1
	v_bfi_b32 v64, s84, v64, v66
	v_cvt_pk_bf16_f32 v0, v0, v1
	v_mul_f32_e32 v1, v67, v2
	v_mul_f32_e32 v2, v67, v3
	v_ashrrev_i32_e32 v65, 31, v64
	v_cvt_pk_bf16_f32 v1, v1, v2
	v_mul_f32_e32 v2, v67, v4
	v_mul_f32_e32 v3, v67, v5
	v_lshlrev_b64 v[64:65], 12, v[64:65]
	v_lshrrev_b32_e32 v66, 1, v66
	v_cvt_pk_bf16_f32 v2, v2, v3
	v_mul_f32_e32 v3, v67, v6
	v_lshl_add_u64 v[64:65], s[8:9], 0, v[64:65]
	v_and_b32_e32 v128, 16, v66
	v_mul_f32_e32 v4, v67, v7
	v_cvt_pk_bf16_f32 v3, v3, v4
	v_lshl_add_u64 v[64:65], v[64:65], 0, v[128:129]
	v_permlane32_swap_b32_e32 v0, v2
	v_permlane32_swap_b32_e32 v1, v3
	global_store_dwordx4 v[64:65], v[0:3], off
	v_mul_f32_e32 v4, v67, v15
	v_mfma_f32_32x32x16_bf16 v[16:31], v[86:89], v[68:71], v[16:31]
	v_mul_f32_e32 v0, v67, v8
	v_mul_f32_e32 v1, v67, v9
	v_cvt_pk_bf16_f32 v0, v0, v1
	v_mul_f32_e32 v1, v67, v10
	v_mul_f32_e32 v2, v67, v11
	v_cvt_pk_bf16_f32 v1, v1, v2
	v_mul_f32_e32 v2, v67, v12
	v_mul_f32_e32 v3, v67, v13
	v_cvt_pk_bf16_f32 v2, v2, v3
	v_mul_f32_e32 v3, v67, v14
	v_cvt_pk_bf16_f32 v3, v3, v4
	v_permlane32_swap_b32_e32 v0, v2
	s_nop 0
	v_permlane32_swap_b32_e32 v1, v3
	global_store_dwordx4 v[64:65], v[0:3], off offset:32
	v_mul_f32_e32 v4, v67, v55
	v_mfma_f32_32x32x16_bf16 v[16:31], v[90:93], v[72:75], v[16:31]
	v_mul_f32_e32 v0, v67, v48
	v_mul_f32_e32 v1, v67, v49
	v_cvt_pk_bf16_f32 v0, v0, v1
	v_mul_f32_e32 v1, v67, v50
	v_mul_f32_e32 v2, v67, v51
	v_cvt_pk_bf16_f32 v1, v1, v2
	v_mul_f32_e32 v2, v67, v52
	v_mul_f32_e32 v3, v67, v53
	v_cvt_pk_bf16_f32 v2, v2, v3
	v_mul_f32_e32 v3, v67, v54
	v_cvt_pk_bf16_f32 v3, v3, v4
	v_permlane32_swap_b32_e32 v0, v2
	s_nop 0
	v_permlane32_swap_b32_e32 v1, v3
	global_store_dwordx4 v[64:65], v[0:3], off offset:64
	v_mul_f32_e32 v4, v67, v63
	v_mfma_f32_32x32x16_bf16 v[16:31], v[94:97], v[76:79], v[16:31]
	v_mul_f32_e32 v0, v67, v56
	v_mul_f32_e32 v1, v67, v57
	v_cvt_pk_bf16_f32 v0, v0, v1
	v_mul_f32_e32 v1, v67, v58
	v_mul_f32_e32 v2, v67, v59
	v_cvt_pk_bf16_f32 v1, v1, v2
	v_mul_f32_e32 v2, v67, v60
	v_mul_f32_e32 v3, v67, v61
	v_cvt_pk_bf16_f32 v2, v2, v3
	v_mul_f32_e32 v3, v67, v62
	v_cvt_pk_bf16_f32 v3, v3, v4
	v_permlane32_swap_b32_e32 v0, v2
	s_nop 0
	v_permlane32_swap_b32_e32 v1, v3
	global_store_dwordx4 v[64:65], v[0:3], off offset:96
	v_mul_f32_e32 v4, v67, v39
	s_lshl_b32 s2, s20, 8
	v_mul_f32_e32 v0, v67, v32
	v_mul_f32_e32 v1, v67, v33
	v_cvt_pk_bf16_f32 v0, v0, v1
	v_mul_f32_e32 v1, v67, v34
	v_mul_f32_e32 v2, v67, v35
	v_cvt_pk_bf16_f32 v1, v1, v2
	v_mul_f32_e32 v2, v67, v36
	v_mul_f32_e32 v3, v67, v37
	v_cvt_pk_bf16_f32 v2, v2, v3
	v_mul_f32_e32 v3, v67, v38
	v_cvt_pk_bf16_f32 v3, v3, v4
	v_permlane32_swap_b32_e32 v0, v2
	s_nop 0
	v_permlane32_swap_b32_e32 v1, v3
	global_store_dwordx4 v[64:65], v[0:3], off offset:128
	v_mul_f32_e32 v4, v67, v47
	s_add_i32 s3, s2, s94
	v_mul_f32_e32 v0, v67, v40
	v_mul_f32_e32 v1, v67, v41
	v_cvt_pk_bf16_f32 v0, v0, v1
	v_mul_f32_e32 v1, v67, v42
	v_mul_f32_e32 v2, v67, v43
	v_cvt_pk_bf16_f32 v1, v1, v2
	v_mul_f32_e32 v2, v67, v44
	v_mul_f32_e32 v3, v67, v45
	v_cvt_pk_bf16_f32 v2, v2, v3
	v_mul_f32_e32 v3, v67, v46
	v_cvt_pk_bf16_f32 v3, v3, v4
	v_permlane32_swap_b32_e32 v0, v2
	s_nop 0
	v_permlane32_swap_b32_e32 v1, v3
	global_store_dwordx4 v[64:65], v[0:3], off offset:160
	v_mul_f32_e32 v4, v67, v23
	s_cmp_lt_i32 s3, s37
	v_mul_f32_e32 v0, v67, v16
	v_mul_f32_e32 v1, v67, v17
	v_cvt_pk_bf16_f32 v0, v0, v1
	v_mul_f32_e32 v1, v67, v18
	v_mul_f32_e32 v2, v67, v19
	v_cvt_pk_bf16_f32 v1, v1, v2
	v_mul_f32_e32 v2, v67, v20
	v_mul_f32_e32 v3, v67, v21
	v_cvt_pk_bf16_f32 v2, v2, v3
	v_mul_f32_e32 v3, v67, v22
	v_cvt_pk_bf16_f32 v3, v3, v4
	v_permlane32_swap_b32_e32 v0, v2
	s_nop 0
	v_permlane32_swap_b32_e32 v1, v3
	global_store_dwordx4 v[64:65], v[0:3], off offset:192
	v_mul_f32_e32 v4, v67, v31
	s_movk_i32 s33, 0xffef
	v_mul_f32_e32 v0, v67, v24
	v_mul_f32_e32 v1, v67, v25
	v_cvt_pk_bf16_f32 v0, v0, v1
	v_mul_f32_e32 v1, v67, v26
	v_mul_f32_e32 v2, v67, v27
	v_cvt_pk_bf16_f32 v1, v1, v2
	v_mul_f32_e32 v2, v67, v28
	v_mul_f32_e32 v3, v67, v29
	v_cvt_pk_bf16_f32 v2, v2, v3
	v_mul_f32_e32 v3, v67, v30
	v_cvt_pk_bf16_f32 v3, v3, v4
	v_permlane32_swap_b32_e32 v0, v2
	s_nop 0
	v_permlane32_swap_b32_e32 v1, v3
	global_store_dwordx4 v[64:65], v[0:3], off offset:224
	s_cbranch_scc0 .LBB0_889

.LBB0_880:
	v_add_u32_e32 v21, 32, v185
	v_and_b32_e32 v17, 0xfffff0, v185
	v_lshlrev_b32_e32 v18, 1, v185
	v_and_b32_e32 v22, 0xfffff0, v21
	v_lshlrev_b32_e32 v23, 1, v21
	v_and_b32_e32 v16, 63, v184
	v_and_or_b32 v17, v18, 8, v17
	v_and_or_b32 v22, v23, 8, v22
	v_lshrrev_b32_e32 v17, 1, v17
	v_lshrrev_b32_e32 v19, 5, v186
	v_lshrrev_b32_e32 v22, 1, v22
	v_lshlrev_b32_e32 v23, 4, v16
	v_lshrrev_b32_e32 v18, 1, v185
	v_or_b32_e32 v17, v17, v19
	v_and_b32_e32 v20, 3, v185
	v_or_b32_e32 v19, v22, v19
	v_lshlrev_b32_e32 v22, 3, v16
	v_and_b32_e32 v23, 0xc0, v23
	v_lshlrev_b32_e32 v16, 1, v16
	v_and_or_b32 v18, v18, 4, v20
	v_lshlrev_b32_e32 v20, 1, v186
	v_and_or_b32 v23, v22, 24, v23
	v_and_b32_e32 v16, 32, v16
	v_and_b32_e32 v22, 0x100, v22
	v_lshlrev_b32_e32 v17, 9, v17
	v_lshlrev_b32_e32 v18, 6, v18
	v_or3_b32 v114, v23, v16, v22
	v_and_b32_e32 v16, 48, v20
	v_or3_b32 v17, v17, v18, v16
	v_add_u32_e32 v212, 0, v17
	v_lshrrev_b32_e32 v22, 3, v212
	v_xor_b32_e32 v22, v22, v212
	v_and_b32_e32 v22, 0x100, v22
	v_lshl_or_b32 v23, v22, 3, v22
	v_xor_b32_e32 v212, v212, v23
	v_lshlrev_b32_e32 v19, 9, v19
	v_cvt_pk_bf16_f32 v138, v176, v177
	v_cvt_pk_bf16_f32 v139, v170, v171
	v_cvt_pk_bf16_f32 v140, v164, v165
	v_cvt_pk_bf16_f32 v141, v144, v145
	v_cvt_pk_bf16_f32 v154, v142, v143
	v_cvt_pk_bf16_f32 v155, v136, v137
	v_cvt_pk_bf16_f32 v156, v134, v135
	v_cvt_pk_bf16_f32 v157, v132, v133
	v_cvt_pk_bf16_f32 v158, v130, v131
	v_cvt_pk_bf16_f32 v159, v126, v127
	v_cvt_pk_bf16_f32 v160, v124, v125
	v_cvt_pk_bf16_f32 v161, v122, v123
	v_cvt_pk_bf16_f32 v150, v120, v121
	v_cvt_pk_bf16_f32 v151, v118, v119
	v_cvt_pk_bf16_f32 v152, v116, v117
	v_cvt_pk_bf16_f32 v153, v112, v113
	v_cvt_pk_bf16_f32 v146, v108, v109
	v_cvt_pk_bf16_f32 v147, v110, v111
	v_cvt_pk_bf16_f32 v148, v104, v105
	v_cvt_pk_bf16_f32 v149, v106, v107
	v_cvt_pk_bf16_f32 v142, v100, v101
	v_cvt_pk_bf16_f32 v143, v102, v103
	v_cvt_pk_bf16_f32 v144, v96, v97
	v_cvt_pk_bf16_f32 v145, v98, v99
	v_cvt_pk_bf16_f32 v134, v92, v93
	v_cvt_pk_bf16_f32 v135, v94, v95
	v_cvt_pk_bf16_f32 v136, v88, v89
	v_cvt_pk_bf16_f32 v137, v90, v91
	v_cvt_pk_bf16_f32 v130, v84, v85
	v_cvt_pk_bf16_f32 v131, v86, v87
	v_cvt_pk_bf16_f32 v132, v80, v81
	v_cvt_pk_bf16_f32 v133, v82, v83
	s_waitcnt vmcnt(0)
	ds_write_b128 v212, v[8:11]
	v_lshlrev_b32_e32 v8, 8, v185
	v_and_b32_e32 v9, 0x70, v184
	v_or3_b32 v16, v19, v18, v16
	v_bitop3_b32 v8, v20, v8, v9 bitop3:0xde
	v_add_u32_e32 v213, 0, v16
	v_lshrrev_b32_e32 v16, 3, v213
	v_xor_b32_e32 v16, v16, v213
	v_and_b32_e32 v16, 0x100, v16
	v_lshl_or_b32 v17, v16, 3, v16
	v_xor_b32_e32 v213, v213, v17
	v_add_u32_e32 v214, 0, v8
	ds_write_b128 v213, v[12:15]
	ds_write_b128 v214, v[4:7] offset:32768
	v_lshlrev_b32_e32 v4, 8, v21
	v_bitop3_b32 v4, v20, v4, v9 bitop3:0xde
	v_add_u32_e32 v215, 0, v4
	ds_write_b128 v215, v[0:3] offset:32768
	v_lshlrev_b32_e32 v0, 4, v163
	v_lshlrev_b32_e32 v56, 8, v163
	v_and_b32_e32 v57, 0x70, v0
	v_bitop3_b32 v0, v162, v56, v57 bitop3:0xde
	v_add_u32_e32 v216, 0, v0
	s_waitcnt lgkmcnt(0)
	s_barrier
	ds_read_b128 v[16:19], v216 offset:32768
	ds_read_b128 v[20:23], v216 offset:40960
	s_waitcnt lgkmcnt(1)
	v_mfma_f32_32x32x16_bf16 v[32:47], v[16:19], v[138:141], 0
	v_or_b32_e32 v48, 32, v162
	v_bitop3_b32 v48, v48, v56, v57 bitop3:0xde
	v_add_u32_e32 v218, 0, v48
	ds_read_b128 v[48:51], v218 offset:32768
	ds_read_b128 v[52:55], v218 offset:40960
	s_cmp_lg_u32 0, -1
	s_cselect_b32 s53, 0, 0
	s_add_u32 s16, s10, s96
	s_waitcnt lgkmcnt(2)
	v_mfma_f32_32x32x16_bf16 v[16:31], v[20:23], v[138:141], 0
	s_addc_u32 s17, s11, s97
	v_mov_b32_e32 v199, v129
	s_add_u32 s18, s8, s96
	s_addc_u32 s19, s9, s97
	v_lshl_add_u64 v[60:61], s[18:19], 0, v[198:199]
	s_add_u32 s2, s16, s96
	s_addc_u32 s3, s17, s97
	s_waitcnt lgkmcnt(1)
	v_mfma_f32_32x32x16_bf16 v[32:47], v[48:51], v[154:157], v[32:47]
	v_or_b32_e32 v48, 64, v162
	v_bitop3_b32 v48, v48, v56, v57 bitop3:0xde
	v_add_u32_e32 v219, 0, v48
	v_lshl_add_u64 v[64:65], s[2:3], 0, v[128:129]
	s_mov_b32 s72, s73
	s_mov_b32 s74, s73
	s_mov_b32 s75, s73
	s_waitcnt lgkmcnt(0)
	v_mfma_f32_32x32x16_bf16 v[16:31], v[52:55], v[154:157], v[16:31]
	ds_read_b128 v[48:51], v219 offset:32768
	ds_read_b128 v[52:55], v219 offset:40960
	s_mov_b32 s76, s73
	s_mov_b32 s77, s73
	s_mov_b32 s78, s73
	s_mov_b32 s79, s73
	s_mov_b32 s80, s73
	s_mov_b32 s81, s73
	s_waitcnt lgkmcnt(1)
	v_mfma_f32_32x32x16_bf16 v[32:47], v[48:51], v[158:161], v[32:47]
	v_or_b32_e32 v48, 0x60, v162
	v_bitop3_b32 v48, v48, v56, v57 bitop3:0xde
	v_add_u32_e32 v220, 0, v48
	s_mov_b32 s82, s73
	s_mov_b32 s83, s73
	s_mov_b32 s84, s73
	s_mov_b32 s85, s73
	s_waitcnt lgkmcnt(0)
	v_mfma_f32_32x32x16_bf16 v[16:31], v[52:55], v[158:161], v[16:31]
	ds_read_b128 v[48:51], v220 offset:32768
	ds_read_b128 v[52:55], v220 offset:40960
	s_mov_b32 s86, s73
	s_mov_b32 s87, s73
	v_mov_b64_e32 v[0:1], s[72:73]
	v_mov_b64_e32 v[14:15], s[86:87]
	v_add_u32_e32 v209, s53, v114
	v_mov_b64_e32 v[2:3], s[74:75]
	s_waitcnt lgkmcnt(1)
	v_mfma_f32_32x32x16_bf16 v[32:47], v[48:51], v[150:153], v[32:47]
	v_or_b32_e32 v48, 0x80, v162
	v_bitop3_b32 v48, v48, v56, v57 bitop3:0xde
	v_add_u32_e32 v221, 0, v48
	v_mov_b64_e32 v[4:5], s[76:77]
	v_mov_b64_e32 v[6:7], s[78:79]
	v_mov_b64_e32 v[8:9], s[80:81]
	v_mov_b64_e32 v[10:11], s[82:83]
	s_waitcnt lgkmcnt(0)
	v_mfma_f32_32x32x16_bf16 v[16:31], v[52:55], v[150:153], v[16:31]
	ds_read_b128 v[48:51], v221 offset:32768
	ds_read_b128 v[52:55], v221 offset:40960
	v_mov_b64_e32 v[12:13], s[84:85]
	s_mov_b32 s39, 4
	v_mov_b32_e32 v217, 0
	v_readlane_b32 s80, v255, 48
	s_movk_i32 s79, 0xff
	s_movk_i32 s84, 0xffe0
	s_waitcnt lgkmcnt(1)
	v_mfma_f32_32x32x16_bf16 v[32:47], v[48:51], v[146:149], v[32:47]
	v_or_b32_e32 v48, 0xa0, v162
	v_bitop3_b32 v48, v48, v56, v57 bitop3:0xde
	v_add_u32_e32 v222, 0, v48
	s_waitcnt lgkmcnt(0)
	v_mfma_f32_32x32x16_bf16 v[16:31], v[52:55], v[146:149], v[16:31]
	ds_read_b128 v[48:51], v222 offset:32768
	ds_read_b128 v[52:55], v222 offset:40960
	s_waitcnt lgkmcnt(1)
	v_mfma_f32_32x32x16_bf16 v[32:47], v[48:51], v[142:145], v[32:47]
	v_or_b32_e32 v48, 0xc0, v162
	v_bitop3_b32 v48, v48, v56, v57 bitop3:0xde
	v_add_u32_e32 v224, 0, v48
	s_waitcnt lgkmcnt(0)
	v_mfma_f32_32x32x16_bf16 v[16:31], v[52:55], v[142:145], v[16:31]
	ds_read_b128 v[48:51], v224 offset:32768
	ds_read_b128 v[52:55], v224 offset:40960
	s_waitcnt lgkmcnt(1)
	v_mfma_f32_32x32x16_bf16 v[32:47], v[48:51], v[134:137], v[32:47]
	v_or_b32_e32 v48, 0xe0, v162
	v_bitop3_b32 v48, v48, v56, v57 bitop3:0xde
	v_add_u32_e32 v223, 0, v48
	v_lshl_add_u64 v[56:57], s[18:19], 0, v[128:129]
	s_waitcnt lgkmcnt(0)
	v_mfma_f32_32x32x16_bf16 v[16:31], v[52:55], v[134:137], v[16:31]
	ds_read_b128 v[48:51], v223 offset:32768
	ds_read_b128 v[52:55], v223 offset:40960
	global_load_dwordx4 v[56:59], v[56:57], off
	s_nop 0
	global_load_dwordx4 v[60:63], v[60:61], off
	s_nop 0
	global_load_dwordx4 v[162:165], v[64:65], off
	v_lshl_add_u64 v[64:65], s[2:3], 0, v[198:199]
	s_waitcnt lgkmcnt(1)
	v_mfma_f32_32x32x16_bf16 v[32:47], v[48:51], v[130:133], v[32:47]
	global_load_dwordx4 v[166:169], v[64:65], off
	s_waitcnt lgkmcnt(0)
	v_mfma_f32_32x32x16_bf16 v[16:31], v[52:55], v[130:133], v[16:31]
	s_nop 8
	v_lshl_add_u64 v[48:49], s[16:17], 0, v[128:129]
	global_load_dwordx4 v[48:51], v[48:49], off
	v_lshl_add_u64 v[52:53], s[16:17], 0, v[198:199]
	global_load_dwordx4 v[52:55], v[52:53], off
	s_add_u32 s16, s18, s96
	s_addc_u32 s17, s19, s97
	v_lshl_add_u64 v[64:65], s[16:17], 0, v[128:129]
	global_load_dwordx4 v[170:173], v[64:65], off
	v_lshl_add_u64 v[64:65], s[16:17], 0, v[198:199]
	global_load_dwordx4 v[174:177], v[64:65], off
	s_and_b64 s[2:3], s[14:15], exec
	s_cselect_b32 s14, 3, 35
	s_waitcnt vmcnt(4)
	s_waitcnt vmcnt(3)
	ds_write_b128 v212, v[48:51] offset:16384
	s_waitcnt vmcnt(2)
	ds_write_b128 v213, v[52:55] offset:16384
	ds_write_b128 v214, v[56:59] offset:49152
	ds_write_b128 v215, v[60:63] offset:49152
	v_exp_f32_e32 v64, v32
	v_exp_f32_e32 v65, v33
	v_exp_f32_e32 v66, v34
	v_exp_f32_e32 v67, v35
	v_exp_f32_e32 v68, v36
	v_exp_f32_e32 v69, v37
	v_exp_f32_e32 v70, v38
	v_exp_f32_e32 v71, v39
	v_exp_f32_e32 v72, v40
	v_exp_f32_e32 v73, v41
	v_exp_f32_e32 v74, v42
	v_exp_f32_e32 v80, v16
	v_exp_f32_e32 v81, v17
	v_exp_f32_e32 v75, v43
	v_exp_f32_e32 v76, v44
	v_exp_f32_e32 v77, v45
	v_exp_f32_e32 v78, v46
	v_exp_f32_e32 v79, v47
	v_exp_f32_e32 v82, v18
	v_exp_f32_e32 v83, v19
	v_lshl_add_u64 v[16:17], s[12:13], 0, v[128:129]
	v_lshl_add_u64 v[18:19], s[12:13], 0, v[198:199]
	v_exp_f32_e32 v94, v30
	v_exp_f32_e32 v95, v31
	v_exp_f32_e32 v92, v28
	v_exp_f32_e32 v93, v29
	v_exp_f32_e32 v196, v26
	v_exp_f32_e32 v197, v27
	v_exp_f32_e32 v194, v24
	v_exp_f32_e32 v195, v25
	v_exp_f32_e32 v86, v22
	v_exp_f32_e32 v87, v23
	v_exp_f32_e32 v84, v20
	v_exp_f32_e32 v85, v21
	s_addk_i32 s53, 0x4000
	v_lshl_add_u64 v[200:201], s[64:65], 0, v[16:17]
	v_lshl_add_u64 v[202:203], s[64:65], 0, v[18:19]
	v_lshl_add_u64 v[204:205], s[66:67], 0, v[16:17]
	v_lshl_add_u64 v[206:207], s[66:67], 0, v[18:19]
	v_mov_b64_e32 v[62:63], v[14:15]
	v_mov_b64_e32 v[46:47], v[14:15]
	v_mov_b64_e32 v[30:31], v[14:15]
	v_add_u32_e32 v211, s53, v114
	v_mov_b64_e32 v[60:61], v[12:13]
	v_mov_b64_e32 v[58:59], v[10:11]
	v_mov_b64_e32 v[56:57], v[8:9]
	v_mov_b64_e32 v[54:55], v[6:7]
	v_mov_b64_e32 v[52:53], v[4:5]
	v_mov_b64_e32 v[50:51], v[2:3]
	v_mov_b64_e32 v[48:49], v[0:1]
	v_mov_b64_e32 v[44:45], v[12:13]
	v_mov_b64_e32 v[42:43], v[10:11]
	v_mov_b64_e32 v[40:41], v[8:9]
	v_mov_b64_e32 v[38:39], v[6:7]
	v_mov_b64_e32 v[36:37], v[4:5]
	v_mov_b64_e32 v[34:35], v[2:3]
	v_mov_b64_e32 v[32:33], v[0:1]
	v_mov_b64_e32 v[28:29], v[12:13]
	v_mov_b64_e32 v[26:27], v[10:11]
	v_mov_b64_e32 v[24:25], v[8:9]
	v_mov_b64_e32 v[22:23], v[6:7]
	v_mov_b64_e32 v[20:21], v[4:5]
	v_mov_b64_e32 v[18:19], v[2:3]
	v_mov_b64_e32 v[16:17], v[0:1]
	s_mov_b32 s53, 0x38e38e39
	s_waitcnt lgkmcnt(0)
	s_barrier
.LBB0_881:
	ds_read_b128 v[96:99], v216 offset:49152
	ds_read_b128 v[100:103], v216 offset:57344
	ds_read_b128 v[178:181], v218 offset:49152
	ds_read_b128 v[182:185], v218 offset:57344
	ds_read_b128 v[240:243], v219 offset:49152
	ds_read_b128 v[244:247], v219 offset:57344
	v_add_f32_e32 v88, v64, v65
	v_add_f32_e32 v89, v72, v73
	v_add_f32_e32 v90, v80, v81
	v_add_f32_e32 v91, v194, v195
	s_waitcnt lgkmcnt(5)
	v_mfma_f32_32x32x16_bf16 v[112:127], v[96:99], v[138:141], 0
	v_add_f32_e32 v88, v66, v88
	v_add_f32_e32 v89, v74, v89
	v_add_f32_e32 v90, v82, v90
	s_waitcnt lgkmcnt(4)
	v_mfma_f32_32x32x16_bf16 v[96:111], v[100:103], v[138:141], 0
	v_add_f32_e32 v91, v196, v91
	v_add_f32_e32 v88, v67, v88
	v_add_f32_e32 v89, v75, v89
	v_add_f32_e32 v90, v83, v90
	s_waitcnt lgkmcnt(3)
	v_mfma_f32_32x32x16_bf16 v[112:127], v[178:181], v[154:157], v[112:127]
	v_add_f32_e32 v91, v197, v91
	v_add_f32_e32 v88, v68, v88
	v_add_f32_e32 v89, v76, v89
	s_waitcnt lgkmcnt(2)
	v_mfma_f32_32x32x16_bf16 v[96:111], v[182:185], v[154:157], v[96:111]
	ds_read_b128 v[178:181], v220 offset:49152
	ds_read_b128 v[182:185], v220 offset:57344
	v_add_f32_e32 v90, v84, v90
	v_add_f32_e32 v91, v92, v91
	v_add_f32_e32 v88, v69, v88
	v_add_f32_e32 v89, v77, v89
	s_waitcnt lgkmcnt(3)
	v_mfma_f32_32x32x16_bf16 v[112:127], v[240:243], v[158:161], v[112:127]
	v_add_f32_e32 v90, v85, v90
	v_add_f32_e32 v91, v93, v91
	v_add_f32_e32 v88, v70, v88
	s_waitcnt lgkmcnt(2)
	v_mfma_f32_32x32x16_bf16 v[96:111], v[244:247], v[158:161], v[96:111]
	ds_read_b128 v[240:243], v221 offset:49152
	ds_read_b128 v[244:247], v221 offset:57344
	v_add_f32_e32 v89, v78, v89
	v_add_f32_e32 v90, v86, v90
	v_add_f32_e32 v91, v94, v91
	v_add_f32_e32 v88, v71, v88
	s_waitcnt lgkmcnt(3)
	v_mfma_f32_32x32x16_bf16 v[112:127], v[178:181], v[150:153], v[112:127]
	v_add_f32_e32 v89, v79, v89
	v_add_f32_e32 v90, v87, v90
	v_add_f32_e32 v91, v95, v91
	s_waitcnt lgkmcnt(2)
	v_mfma_f32_32x32x16_bf16 v[96:111], v[182:185], v[150:153], v[96:111]
	ds_read_b128 v[178:181], v222 offset:49152
	ds_read_b128 v[182:185], v222 offset:57344
	v_add_f32_e32 v88, v89, v88
	v_add_f32_e32 v89, v91, v90
	v_add_f32_e32 v227, v88, v89
	v_mov_b32_e32 v228, v227
	s_waitcnt lgkmcnt(3)
	v_mfma_f32_32x32x16_bf16 v[112:127], v[240:243], v[146:149], v[112:127]
	v_cvt_pk_bf16_f32 v88, v64, v65
	v_cvt_pk_bf16_f32 v89, v66, v67
	v_cvt_pk_bf16_f32 v90, v68, v69
	v_cvt_pk_bf16_f32 v91, v70, v71
	s_waitcnt lgkmcnt(2)
	v_mfma_f32_32x32x16_bf16 v[96:111], v[244:247], v[146:149], v[96:111]
	ds_read_b128 v[240:243], v224 offset:49152
	ds_read_b128 v[244:247], v224 offset:57344
	v_permlane32_swap_b32_e32 v227, v228
	s_waitcnt lgkmcnt(3)
	v_mfma_f32_32x32x16_bf16 v[112:127], v[178:181], v[142:145], v[112:127]
	v_cvt_pk_bf16_f32 v72, v72, v73
	v_cvt_pk_bf16_f32 v73, v74, v75
	v_cvt_pk_bf16_f32 v74, v76, v77
	v_cvt_pk_bf16_f32 v75, v78, v79
	s_waitcnt lgkmcnt(2)
	v_mfma_f32_32x32x16_bf16 v[96:111], v[182:185], v[142:145], v[96:111]
	ds_read_b128 v[178:181], v223 offset:49152
	ds_read_b128 v[182:185], v223 offset:57344
	v_cvt_pk_bf16_f32 v64, v80, v81
	v_cvt_pk_bf16_f32 v65, v82, v83
	v_cvt_pk_bf16_f32 v66, v84, v85
	s_waitcnt lgkmcnt(3)
	v_mfma_f32_32x32x16_bf16 v[112:127], v[240:243], v[134:137], v[112:127]
	v_cvt_pk_bf16_f32 v67, v86, v87
	v_cvt_pk_bf16_f32 v68, v194, v195
	v_cvt_pk_bf16_f32 v69, v196, v197
	v_cvt_pk_bf16_f32 v70, v92, v93
	s_waitcnt lgkmcnt(2)
	v_mfma_f32_32x32x16_bf16 v[96:111], v[244:247], v[134:137], v[96:111]
	v_cvt_pk_bf16_f32 v71, v94, v95
	s_waitcnt lgkmcnt(1)
	v_mfma_f32_32x32x16_bf16 v[112:127], v[178:181], v[130:133], v[112:127]
	s_waitcnt lgkmcnt(0)
	v_mfma_f32_32x32x16_bf16 v[96:111], v[182:185], v[130:133], v[96:111]
	s_add_i32 s2, s39, -1
	s_mul_i32 s2, s2, s62
	s_lshl_b32 s72, s2, 6
	s_lshl_b64 s[2:3], s[72:73], 1
	s_add_u32 s12, s10, s2
	s_addc_u32 s13, s11, s3
	s_add_u32 s2, s8, s2
	s_addc_u32 s3, s9, s3
	global_load_dwordx4 v[178:181], v128, s[12:13]
	global_load_dwordx4 v[182:185], v198, s[12:13]
	global_load_dwordx4 v[186:189], v128, s[2:3]
	global_load_dwordx4 v[190:193], v198, s[2:3]
	ds_read_b64_tr_b16 v[76:77], v209 offset:0
	ds_read_b64_tr_b16 v[78:79], v209 offset:0x800
	ds_read_b64_tr_b16 v[80:81], v209 offset:0x1000
	ds_read_b64_tr_b16 v[82:83], v209 offset:0x1800
	ds_read_b64_tr_b16 v[84:85], v209 offset:0x2000
	ds_read_b64_tr_b16 v[86:87], v209 offset:0x2800
	ds_read_b64_tr_b16 v[92:93], v209 offset:0x3000
	ds_read_b64_tr_b16 v[94:95], v209 offset:0x3800
	s_waitcnt lgkmcnt(0)
	s_nop 0
	v_mfma_f32_32x32x16_bf16 v[0:15], v[76:79], v[88:91], v[0:15]
	v_mfma_f32_32x32x16_bf16 v[0:15], v[80:83], v[72:75], v[0:15]
	v_mfma_f32_32x32x16_bf16 v[0:15], v[84:87], v[64:67], v[0:15]
	ds_read_b64_tr_b16 v[76:77], v209 offset:0x200
	ds_read_b64_tr_b16 v[78:79], v209 offset:0xa00
	ds_read_b64_tr_b16 v[80:81], v209 offset:0x1200
	v_mfma_f32_32x32x16_bf16 v[0:15], v[92:95], v[68:71], v[0:15]
	ds_read_b64_tr_b16 v[82:83], v209 offset:0x1a00
	ds_read_b64_tr_b16 v[84:85], v209 offset:0x2200
	ds_read_b64_tr_b16 v[86:87], v209 offset:0x2a00
	ds_read_b64_tr_b16 v[92:93], v209 offset:0x3200
	ds_read_b64_tr_b16 v[94:95], v209 offset:0x3a00
	s_waitcnt lgkmcnt(0)
	v_mfma_f32_32x32x16_bf16 v[48:63], v[76:79], v[88:91], v[48:63]
	v_mfma_f32_32x32x16_bf16 v[48:63], v[80:83], v[72:75], v[48:63]
	v_mfma_f32_32x32x16_bf16 v[48:63], v[84:87], v[64:67], v[48:63]
	ds_read_b64_tr_b16 v[76:77], v209 offset:0x400
	ds_read_b64_tr_b16 v[78:79], v209 offset:0xc00
	ds_read_b64_tr_b16 v[80:81], v209 offset:0x1400
	ds_read_b64_tr_b16 v[82:83], v209 offset:0x1c00
	v_mfma_f32_32x32x16_bf16 v[48:63], v[92:95], v[68:71], v[48:63]
	ds_read_b64_tr_b16 v[84:85], v209 offset:0x2400
	ds_read_b64_tr_b16 v[86:87], v209 offset:0x2c00
	ds_read_b64_tr_b16 v[92:93], v209 offset:0x3400
	ds_read_b64_tr_b16 v[94:95], v209 offset:0x3c00
	s_waitcnt lgkmcnt(0)
	v_mfma_f32_32x32x16_bf16 v[32:47], v[76:79], v[88:91], v[32:47]
	ds_read_b64_tr_b16 v[76:77], v209 offset:0x600
	ds_read_b64_tr_b16 v[78:79], v209 offset:0xe00
	v_exp_f32_e32 v234, v104
	v_exp_f32_e32 v235, v105
	v_exp_f32_e32 v236, v106
	v_exp_f32_e32 v237, v107
	v_exp_f32_e32 v238, v108
	v_exp_f32_e32 v239, v109
	v_exp_f32_e32 v231, v110
	v_exp_f32_e32 v249, v111
	v_mfma_f32_32x32x16_bf16 v[32:47], v[80:83], v[72:75], v[32:47]
	v_exp_f32_e32 v80, v112
	v_exp_f32_e32 v81, v113
	v_exp_f32_e32 v82, v114
	v_exp_f32_e32 v83, v115
	v_mfma_f32_32x32x16_bf16 v[32:47], v[84:87], v[64:67], v[32:47]
	v_exp_f32_e32 v84, v116
	v_exp_f32_e32 v85, v117
	v_exp_f32_e32 v86, v118
	v_exp_f32_e32 v87, v119
	v_exp_f32_e32 v112, v96
	v_exp_f32_e32 v113, v97
	v_exp_f32_e32 v114, v98
	v_exp_f32_e32 v115, v99
	v_exp_f32_e32 v116, v100
	v_exp_f32_e32 v117, v101
	v_exp_f32_e32 v118, v102
	v_exp_f32_e32 v119, v103
	v_mfma_f32_32x32x16_bf16 v[32:47], v[92:95], v[68:71], v[32:47]
	ds_read_b64_tr_b16 v[92:93], v209 offset:0x1600
	ds_read_b64_tr_b16 v[94:95], v209 offset:0x1e00
	ds_read_b64_tr_b16 v[96:97], v209 offset:0x2600
	ds_read_b64_tr_b16 v[98:99], v209 offset:0x2e00
	ds_read_b64_tr_b16 v[100:101], v209 offset:0x3600
	ds_read_b64_tr_b16 v[102:103], v209 offset:0x3e00
	s_waitcnt lgkmcnt(0)
	v_mfma_f32_32x32x16_bf16 v[16:31], v[76:79], v[88:91], v[16:31]
	v_exp_f32_e32 v88, v120
	v_exp_f32_e32 v89, v121
	v_exp_f32_e32 v90, v122
	v_exp_f32_e32 v91, v123
	v_mfma_f32_32x32x16_bf16 v[16:31], v[92:95], v[72:75], v[16:31]
	v_exp_f32_e32 v92, v124
	v_exp_f32_e32 v93, v125
	v_exp_f32_e32 v94, v126
	v_exp_f32_e32 v95, v127
	s_barrier
	v_mfma_f32_32x32x16_bf16 v[16:31], v[96:99], v[64:67], v[16:31]
	s_waitcnt vmcnt(4)
	s_waitcnt vmcnt(7)
	ds_write_b128 v212, v[162:165]
	s_waitcnt vmcnt(6)
	ds_write_b128 v213, v[166:169]
	s_waitcnt vmcnt(5)
	ds_write_b128 v214, v[170:173] offset:32768
	s_waitcnt vmcnt(4)
	ds_write_b128 v215, v[174:177] offset:32768
	v_mfma_f32_32x32x16_bf16 v[16:31], v[100:103], v[68:71], v[16:31]
.LBB0_883:
	s_waitcnt lgkmcnt(0)
	s_barrier
	ds_read_b128 v[64:67], v216 offset:32768
	ds_read_b128 v[68:71], v216 offset:40960
	ds_read_b128 v[162:165], v218 offset:32768
	ds_read_b128 v[166:169], v218 offset:40960
	ds_read_b128 v[240:243], v219 offset:32768
	ds_read_b128 v[244:247], v219 offset:40960
	v_add_f32_e32 v120, v80, v81
	v_add_f32_e32 v121, v88, v89
	v_add_f32_e32 v122, v112, v113
	v_add_f32_e32 v123, v234, v235
	s_waitcnt lgkmcnt(5)
	v_mfma_f32_32x32x16_bf16 v[96:111], v[64:67], v[138:141], 0
	v_add_f32_e32 v120, v82, v120
	v_add_f32_e32 v121, v90, v121
	v_add_f32_e32 v122, v114, v122
	s_waitcnt lgkmcnt(4)
	v_mfma_f32_32x32x16_bf16 v[64:79], v[68:71], v[138:141], 0
	v_add_f32_e32 v123, v236, v123
	v_add_f32_e32 v120, v83, v120
	v_add_f32_e32 v121, v91, v121
	v_add_f32_e32 v122, v115, v122
	s_waitcnt lgkmcnt(3)
	v_mfma_f32_32x32x16_bf16 v[96:111], v[162:165], v[154:157], v[96:111]
	v_add_f32_e32 v123, v237, v123
	v_add_f32_e32 v120, v84, v120
	v_add_f32_e32 v121, v92, v121
	s_waitcnt lgkmcnt(2)
	v_mfma_f32_32x32x16_bf16 v[64:79], v[166:169], v[154:157], v[64:79]
	ds_read_b128 v[162:165], v220 offset:32768
	ds_read_b128 v[166:169], v220 offset:40960
	v_add_f32_e32 v122, v116, v122
	v_add_f32_e32 v123, v238, v123
	v_add_f32_e32 v120, v85, v120
	v_add_f32_e32 v121, v93, v121
	s_waitcnt lgkmcnt(3)
	v_mfma_f32_32x32x16_bf16 v[96:111], v[240:243], v[158:161], v[96:111]
	v_add_f32_e32 v122, v117, v122
	v_add_f32_e32 v123, v239, v123
	v_add_f32_e32 v120, v86, v120
	s_waitcnt lgkmcnt(2)
	v_mfma_f32_32x32x16_bf16 v[64:79], v[244:247], v[158:161], v[64:79]
	ds_read_b128 v[240:243], v221 offset:32768
	ds_read_b128 v[244:247], v221 offset:40960
	v_add_f32_e32 v121, v94, v121
	v_add_f32_e32 v122, v118, v122
	v_add_f32_e32 v123, v231, v123
	v_add_f32_e32 v120, v87, v120
	s_waitcnt lgkmcnt(3)
	v_mfma_f32_32x32x16_bf16 v[96:111], v[162:165], v[150:153], v[96:111]
	v_add_f32_e32 v121, v95, v121
	v_add_f32_e32 v122, v119, v122
	v_add_f32_e32 v123, v249, v123
	s_waitcnt lgkmcnt(2)
	v_mfma_f32_32x32x16_bf16 v[64:79], v[166:169], v[150:153], v[64:79]
	ds_read_b128 v[162:165], v222 offset:32768
	ds_read_b128 v[166:169], v222 offset:40960
	v_add_f32_e32 v120, v121, v120
	v_add_f32_e32 v121, v123, v122
	v_add_f32_e32 v229, v120, v121
	v_mov_b32_e32 v233, v229
	s_waitcnt lgkmcnt(3)
	v_mfma_f32_32x32x16_bf16 v[96:111], v[240:243], v[146:149], v[96:111]
	v_permlane32_swap_b32_e32 v229, v233
	v_cvt_pk_bf16_f32 v124, v80, v81
	v_cvt_pk_bf16_f32 v125, v82, v83
	v_cvt_pk_bf16_f32 v126, v84, v85
	s_waitcnt lgkmcnt(2)
	v_mfma_f32_32x32x16_bf16 v[64:79], v[244:247], v[146:149], v[64:79]
	ds_read_b128 v[240:243], v224 offset:32768
	ds_read_b128 v[244:247], v224 offset:40960
	v_cvt_pk_bf16_f32 v127, v86, v87
	v_cvt_pk_bf16_f32 v120, v88, v89
	v_cvt_pk_bf16_f32 v121, v90, v91
	s_waitcnt lgkmcnt(3)
	v_mfma_f32_32x32x16_bf16 v[96:111], v[162:165], v[142:145], v[96:111]
	v_cvt_pk_bf16_f32 v122, v92, v93
	v_cvt_pk_bf16_f32 v123, v94, v95
	v_cvt_pk_bf16_f32 v112, v112, v113
	v_cvt_pk_bf16_f32 v113, v114, v115
	s_waitcnt lgkmcnt(2)
	v_mfma_f32_32x32x16_bf16 v[64:79], v[166:169], v[142:145], v[64:79]
	ds_read_b128 v[162:165], v223 offset:32768
	ds_read_b128 v[166:169], v223 offset:40960
	v_cvt_pk_bf16_f32 v114, v116, v117
	v_cvt_pk_bf16_f32 v115, v118, v119
	v_cvt_pk_bf16_f32 v116, v234, v235
	s_waitcnt lgkmcnt(3)
	v_mfma_f32_32x32x16_bf16 v[96:111], v[240:243], v[134:137], v[96:111]
	v_cvt_pk_bf16_f32 v117, v236, v237
	v_cvt_pk_bf16_f32 v118, v238, v239
	v_cvt_pk_bf16_f32 v119, v231, v249
	s_waitcnt lgkmcnt(2)
	v_mfma_f32_32x32x16_bf16 v[64:79], v[244:247], v[134:137], v[64:79]
	s_waitcnt lgkmcnt(1)
	v_mfma_f32_32x32x16_bf16 v[96:111], v[162:165], v[130:133], v[96:111]
	s_waitcnt lgkmcnt(0)
	v_mfma_f32_32x32x16_bf16 v[64:79], v[166:169], v[130:133], v[64:79]
	s_min_i32 s2, s39, s14
	s_mul_i32 s2, s2, s62
	s_lshl_b32 s72, s2, 6
	s_lshl_b64 s[2:3], s[72:73], 1
	s_add_u32 s12, s10, s2
	s_addc_u32 s13, s11, s3
	s_add_u32 s2, s8, s2
	s_addc_u32 s3, s9, s3
	global_load_dwordx4 v[162:165], v128, s[12:13]
	global_load_dwordx4 v[166:169], v198, s[12:13]
	global_load_dwordx4 v[170:173], v128, s[2:3]
	global_load_dwordx4 v[174:177], v198, s[2:3]
	ds_read_b64_tr_b16 v[80:81], v211 offset:0
	ds_read_b64_tr_b16 v[82:83], v211 offset:0x800
	ds_read_b64_tr_b16 v[84:85], v211 offset:0x1000
	ds_read_b64_tr_b16 v[86:87], v211 offset:0x1800
	ds_read_b64_tr_b16 v[88:89], v211 offset:0x2000
	ds_read_b64_tr_b16 v[90:91], v211 offset:0x2800
	ds_read_b64_tr_b16 v[92:93], v211 offset:0x3000
	ds_read_b64_tr_b16 v[94:95], v211 offset:0x3800
	s_waitcnt lgkmcnt(0)
	s_nop 0
	v_mfma_f32_32x32x16_bf16 v[0:15], v[80:83], v[124:127], v[0:15]
	v_mfma_f32_32x32x16_bf16 v[0:15], v[84:87], v[120:123], v[0:15]
	v_mfma_f32_32x32x16_bf16 v[0:15], v[88:91], v[112:115], v[0:15]
	ds_read_b64_tr_b16 v[80:81], v211 offset:0x200
	ds_read_b64_tr_b16 v[82:83], v211 offset:0xa00
	ds_read_b64_tr_b16 v[84:85], v211 offset:0x1200
	v_mfma_f32_32x32x16_bf16 v[0:15], v[92:95], v[116:119], v[0:15]
	ds_read_b64_tr_b16 v[86:87], v211 offset:0x1a00
	ds_read_b64_tr_b16 v[88:89], v211 offset:0x2200
	ds_read_b64_tr_b16 v[90:91], v211 offset:0x2a00
	ds_read_b64_tr_b16 v[92:93], v211 offset:0x3200
	ds_read_b64_tr_b16 v[94:95], v211 offset:0x3a00
	s_waitcnt lgkmcnt(0)
	v_mfma_f32_32x32x16_bf16 v[48:63], v[80:83], v[124:127], v[48:63]
	v_mfma_f32_32x32x16_bf16 v[48:63], v[84:87], v[120:123], v[48:63]
	v_mfma_f32_32x32x16_bf16 v[48:63], v[88:91], v[112:115], v[48:63]
	ds_read_b64_tr_b16 v[80:81], v211 offset:0x400
	ds_read_b64_tr_b16 v[82:83], v211 offset:0xc00
	ds_read_b64_tr_b16 v[84:85], v211 offset:0x1400
	ds_read_b64_tr_b16 v[86:87], v211 offset:0x1c00
	v_mfma_f32_32x32x16_bf16 v[48:63], v[92:95], v[116:119], v[48:63]
	ds_read_b64_tr_b16 v[88:89], v211 offset:0x2400
	ds_read_b64_tr_b16 v[90:91], v211 offset:0x2c00
	ds_read_b64_tr_b16 v[92:93], v211 offset:0x3400
	ds_read_b64_tr_b16 v[94:95], v211 offset:0x3c00
	s_waitcnt lgkmcnt(0)
	v_mfma_f32_32x32x16_bf16 v[32:47], v[80:83], v[124:127], v[32:47]
	v_exp_f32_e32 v80, v64
	v_exp_f32_e32 v81, v65
	v_exp_f32_e32 v64, v96
	v_exp_f32_e32 v65, v97
	v_exp_f32_e32 v82, v66
	v_exp_f32_e32 v83, v67
	v_exp_f32_e32 v66, v98
	v_exp_f32_e32 v67, v99
	v_mfma_f32_32x32x16_bf16 v[32:47], v[84:87], v[120:123], v[32:47]
	v_exp_f32_e32 v84, v68
	v_exp_f32_e32 v85, v69
	v_exp_f32_e32 v68, v100
	v_exp_f32_e32 v69, v101
	v_exp_f32_e32 v86, v70
	v_exp_f32_e32 v87, v71
	v_exp_f32_e32 v70, v102
	v_exp_f32_e32 v71, v103
	v_mfma_f32_32x32x16_bf16 v[32:47], v[88:91], v[112:115], v[32:47]
	v_exp_f32_e32 v194, v72
	v_exp_f32_e32 v195, v73
	ds_read_b64_tr_b16 v[72:73], v211 offset:0x600
	v_exp_f32_e32 v196, v74
	v_exp_f32_e32 v197, v75
	ds_read_b64_tr_b16 v[74:75], v211 offset:0xe00
	v_mfma_f32_32x32x16_bf16 v[32:47], v[92:95], v[116:119], v[32:47]
	v_exp_f32_e32 v92, v76
	v_exp_f32_e32 v93, v77
	ds_read_b64_tr_b16 v[76:77], v211 offset:0x1600
	v_exp_f32_e32 v94, v78
	v_exp_f32_e32 v95, v79
	ds_read_b64_tr_b16 v[78:79], v211 offset:0x1e00
	ds_read_b64_tr_b16 v[96:97], v211 offset:0x2600
	ds_read_b64_tr_b16 v[98:99], v211 offset:0x2e00
	ds_read_b64_tr_b16 v[100:101], v211 offset:0x3600
	ds_read_b64_tr_b16 v[102:103], v211 offset:0x3e00
	s_waitcnt lgkmcnt(0)
	v_mfma_f32_32x32x16_bf16 v[16:31], v[72:75], v[124:127], v[16:31]
	v_exp_f32_e32 v72, v104
	v_exp_f32_e32 v73, v105
	v_exp_f32_e32 v74, v106
	v_exp_f32_e32 v75, v107
	v_mfma_f32_32x32x16_bf16 v[16:31], v[76:79], v[120:123], v[16:31]
	v_exp_f32_e32 v76, v108
	v_exp_f32_e32 v77, v109
	v_exp_f32_e32 v78, v110
	v_exp_f32_e32 v79, v111
	s_barrier
	v_mfma_f32_32x32x16_bf16 v[16:31], v[96:99], v[112:115], v[16:31]
	s_waitcnt vmcnt(4)
	s_waitcnt vmcnt(7)
	ds_write_b128 v212, v[178:181] offset:16384
	s_waitcnt vmcnt(6)
	ds_write_b128 v213, v[182:185] offset:16384
	s_waitcnt vmcnt(5)
	ds_write_b128 v214, v[186:189] offset:49152
	s_waitcnt vmcnt(4)
	ds_write_b128 v215, v[190:193] offset:49152
	v_mfma_f32_32x32x16_bf16 v[16:31], v[100:103], v[116:119], v[16:31]

.LBB0_887:
	ds_read_b128 v[96:99], v216 offset:49152
	ds_read_b128 v[100:103], v216 offset:57344
	s_waitcnt lgkmcnt(1)
	v_mfma_f32_32x32x16_bf16 v[112:127], v[96:99], v[138:141], 0
	s_waitcnt lgkmcnt(0)
	v_mfma_f32_32x32x16_bf16 v[96:111], v[100:103], v[138:141], 0
	ds_read_b128 v[138:141], v218 offset:49152
	s_waitcnt vmcnt(3)
	ds_read_b128 v[162:165], v218 offset:57344
	v_add_f32_e32 v128, v64, v65
	v_add_f32_e32 v128, v66, v128
	s_waitcnt lgkmcnt(1)
	v_mfma_f32_32x32x16_bf16 v[112:127], v[138:141], v[154:157], v[112:127]
	v_add_f32_e32 v128, v67, v128
	v_add_f32_e32 v128, v68, v128
	v_add_f32_e32 v128, v69, v128
	v_add_f32_e32 v128, v70, v128
	v_add_f32_e32 v128, v71, v128
	s_waitcnt lgkmcnt(0)
	v_mfma_f32_32x32x16_bf16 v[96:111], v[162:165], v[154:157], v[96:111]
	ds_read_b128 v[138:141], v219 offset:49152
	ds_read_b128 v[154:157], v219 offset:57344
	s_waitcnt lgkmcnt(1)
	v_mfma_f32_32x32x16_bf16 v[112:127], v[138:141], v[158:161], v[112:127]
	s_waitcnt lgkmcnt(0)
	v_mfma_f32_32x32x16_bf16 v[96:111], v[154:157], v[158:161], v[96:111]
	ds_read_b128 v[138:141], v220 offset:49152
	ds_read_b128 v[154:157], v220 offset:57344
	s_waitcnt lgkmcnt(1)
	v_mfma_f32_32x32x16_bf16 v[112:127], v[138:141], v[150:153], v[112:127]
	s_waitcnt lgkmcnt(0)
	v_mfma_f32_32x32x16_bf16 v[96:111], v[154:157], v[150:153], v[96:111]
	ds_read_b128 v[138:141], v221 offset:49152
	ds_read_b128 v[150:153], v221 offset:57344
	s_waitcnt lgkmcnt(1)
	v_mfma_f32_32x32x16_bf16 v[112:127], v[138:141], v[146:149], v[112:127]
	s_waitcnt lgkmcnt(0)
	v_mfma_f32_32x32x16_bf16 v[96:111], v[150:153], v[146:149], v[96:111]
	ds_read_b128 v[138:141], v222 offset:49152
	ds_read_b128 v[146:149], v222 offset:57344
	s_waitcnt lgkmcnt(1)
	v_mfma_f32_32x32x16_bf16 v[112:127], v[138:141], v[142:145], v[112:127]
	s_waitcnt lgkmcnt(0)
	v_mfma_f32_32x32x16_bf16 v[96:111], v[146:149], v[142:145], v[96:111]
	ds_read_b128 v[138:141], v224 offset:49152
	ds_read_b128 v[142:145], v224 offset:57344
	s_waitcnt lgkmcnt(1)
	v_mfma_f32_32x32x16_bf16 v[112:127], v[138:141], v[134:137], v[112:127]
	s_waitcnt lgkmcnt(0)
	v_mfma_f32_32x32x16_bf16 v[96:111], v[142:145], v[134:137], v[96:111]
	ds_read_b128 v[134:137], v223 offset:49152
	ds_read_b128 v[138:141], v223 offset:57344
	s_waitcnt lgkmcnt(1)
	v_mfma_f32_32x32x16_bf16 v[112:127], v[134:137], v[130:133], v[112:127]
	s_waitcnt lgkmcnt(0)
	v_mfma_f32_32x32x16_bf16 v[96:111], v[138:141], v[130:133], v[96:111]
	v_add_f32_e32 v130, v72, v73
	v_add_f32_e32 v131, v80, v81
	v_add_f32_e32 v132, v194, v195
	v_add_f32_e32 v130, v74, v130
	v_add_f32_e32 v131, v82, v131
	v_add_f32_e32 v132, v196, v132
	v_add_f32_e32 v130, v75, v130
	v_add_f32_e32 v131, v83, v131
	v_add_f32_e32 v132, v197, v132
	v_add_f32_e32 v130, v76, v130
	v_add_f32_e32 v131, v84, v131
	v_add_f32_e32 v132, v92, v132
	v_add_f32_e32 v130, v77, v130
	v_add_f32_e32 v131, v85, v131
	v_add_f32_e32 v132, v93, v132
	v_add_f32_e32 v130, v78, v130
	v_add_f32_e32 v131, v86, v131
	v_add_f32_e32 v132, v94, v132
	v_add_f32_e32 v130, v79, v130
	v_add_f32_e32 v131, v87, v131
	v_add_f32_e32 v132, v95, v132
	v_add_f32_e32 v128, v130, v128
	v_add_f32_e32 v130, v132, v131
	v_add_f32_e32 v142, v128, v130
	v_mov_b32_e32 v143, v142
	v_cvt_pk_bf16_f32 v130, v64, v65
	v_cvt_pk_bf16_f32 v131, v66, v67
	v_cvt_pk_bf16_f32 v132, v68, v69
	v_cvt_pk_bf16_f32 v133, v70, v71
	v_cvt_pk_bf16_f32 v72, v72, v73
	v_cvt_pk_bf16_f32 v73, v74, v75
	v_cvt_pk_bf16_f32 v74, v76, v77
	v_cvt_pk_bf16_f32 v75, v78, v79
	s_nop 1
	v_permlane32_swap_b32_e32 v142, v143
	v_cvt_pk_bf16_f32 v138, v80, v81
	v_cvt_pk_bf16_f32 v139, v82, v83
	v_cvt_pk_bf16_f32 v140, v84, v85
	v_cvt_pk_bf16_f32 v141, v86, v87
	v_cvt_pk_bf16_f32 v134, v194, v195
	v_cvt_pk_bf16_f32 v135, v196, v197
	v_cvt_pk_bf16_f32 v136, v92, v93
	v_cvt_pk_bf16_f32 v137, v94, v95
	ds_read_b64_tr_b16 v[64:65], v209 offset:0
	ds_read_b64_tr_b16 v[66:67], v209 offset:0x800
	ds_read_b64_tr_b16 v[68:69], v209 offset:0x1000
	ds_read_b64_tr_b16 v[70:71], v209 offset:0x1800
	ds_read_b64_tr_b16 v[76:77], v209 offset:0x2000
	ds_read_b64_tr_b16 v[78:79], v209 offset:0x2800
	ds_read_b64_tr_b16 v[80:81], v209 offset:0x3000
	ds_read_b64_tr_b16 v[82:83], v209 offset:0x3800
	s_waitcnt lgkmcnt(0)
	s_nop 0
	v_mfma_f32_32x32x16_bf16 v[0:15], v[64:67], v[130:133], v[0:15]
	v_mfma_f32_32x32x16_bf16 v[0:15], v[68:71], v[72:75], v[0:15]
	v_mfma_f32_32x32x16_bf16 v[0:15], v[76:79], v[138:141], v[0:15]
	ds_read_b64_tr_b16 v[64:65], v209 offset:0x200
	ds_read_b64_tr_b16 v[66:67], v209 offset:0xa00
	ds_read_b64_tr_b16 v[68:69], v209 offset:0x1200
	v_mfma_f32_32x32x16_bf16 v[0:15], v[80:83], v[134:137], v[0:15]
	ds_read_b64_tr_b16 v[70:71], v209 offset:0x1a00
	ds_read_b64_tr_b16 v[76:77], v209 offset:0x2200
	ds_read_b64_tr_b16 v[78:79], v209 offset:0x2a00
	ds_read_b64_tr_b16 v[80:81], v209 offset:0x3200
	ds_read_b64_tr_b16 v[82:83], v209 offset:0x3a00
	s_waitcnt lgkmcnt(0)
	v_mfma_f32_32x32x16_bf16 v[48:63], v[64:67], v[130:133], v[48:63]
	v_mfma_f32_32x32x16_bf16 v[48:63], v[68:71], v[72:75], v[48:63]
	v_mfma_f32_32x32x16_bf16 v[48:63], v[76:79], v[138:141], v[48:63]
	v_mov_b32_e32 v128, 1.0
	v_mov_b32_e32 v208, 1.0
	ds_read_b64_tr_b16 v[64:65], v209 offset:0x400
	ds_read_b64_tr_b16 v[66:67], v209 offset:0xc00
	ds_read_b64_tr_b16 v[68:69], v209 offset:0x1400
	v_mfma_f32_32x32x16_bf16 v[48:63], v[80:83], v[134:137], v[48:63]
	ds_read_b64_tr_b16 v[70:71], v209 offset:0x1c00
	ds_read_b64_tr_b16 v[76:77], v209 offset:0x2400
	ds_read_b64_tr_b16 v[78:79], v209 offset:0x2c00
	ds_read_b64_tr_b16 v[80:81], v209 offset:0x3400
	ds_read_b64_tr_b16 v[82:83], v209 offset:0x3c00
	s_waitcnt lgkmcnt(0)
	v_mfma_f32_32x32x16_bf16 v[32:47], v[64:67], v[130:133], v[32:47]
	v_mov_b32_e32 v84, v100
	v_mov_b32_e32 v85, v101
	v_mov_b32_e32 v86, v102
	v_mov_b32_e32 v87, v103
	v_mov_b32_e32 v88, v104
	v_mov_b32_e32 v89, v105
	v_mov_b32_e32 v90, v106
	v_mov_b32_e32 v91, v107
	v_exp_f32_e32 v64, v112
	v_exp_f32_e32 v65, v113
	v_exp_f32_e32 v66, v114
	v_mfma_f32_32x32x16_bf16 v[32:47], v[68:71], v[72:75], v[32:47]
	v_exp_f32_e32 v67, v115
	v_exp_f32_e32 v68, v116
	v_exp_f32_e32 v69, v117
	v_exp_f32_e32 v70, v118
	v_exp_f32_e32 v71, v119
	v_mov_b32_e32 v94, v110
	v_mov_b32_e32 v95, v111
	v_mov_b32_e32 v92, v108
	v_mov_b32_e32 v93, v109
	v_mfma_f32_32x32x16_bf16 v[32:47], v[76:79], v[138:141], v[32:47]
	ds_read_b64_tr_b16 v[76:77], v209 offset:0x600
	ds_read_b64_tr_b16 v[78:79], v209 offset:0xe00
	v_mfma_f32_32x32x16_bf16 v[32:47], v[80:83], v[134:137], v[32:47]
	v_mov_b32_e32 v80, v96
	v_mov_b32_e32 v81, v97
	ds_read_b64_tr_b16 v[96:97], v209 offset:0x1600
	v_mov_b32_e32 v82, v98
	v_mov_b32_e32 v83, v99
	ds_read_b64_tr_b16 v[98:99], v209 offset:0x1e00
	ds_read_b64_tr_b16 v[100:101], v209 offset:0x2600
	ds_read_b64_tr_b16 v[102:103], v209 offset:0x2e00
	ds_read_b64_tr_b16 v[104:105], v209 offset:0x3600
	ds_read_b64_tr_b16 v[106:107], v209 offset:0x3e00
	s_waitcnt lgkmcnt(0)
	v_mfma_f32_32x32x16_bf16 v[16:31], v[76:79], v[130:133], v[16:31]
	v_exp_f32_e32 v76, v124
	v_exp_f32_e32 v77, v125
	v_exp_f32_e32 v78, v126
	v_exp_f32_e32 v79, v127
	v_mfma_f32_32x32x16_bf16 v[16:31], v[96:99], v[72:75], v[16:31]
	v_exp_f32_e32 v72, v120
	v_exp_f32_e32 v73, v121
	v_exp_f32_e32 v74, v122
	v_exp_f32_e32 v75, v123
	s_barrier
	v_mfma_f32_32x32x16_bf16 v[16:31], v[100:103], v[138:141], v[16:31]
	v_mfma_f32_32x32x16_bf16 v[16:31], v[104:107], v[134:137], v[16:31]
	s_branch .LBB0_873
	v_pk_mul_f32 v[14:15], v[14:15], v[128:129] op_sel_hi:[1,0]
	v_pk_mul_f32 v[12:13], v[12:13], v[128:129] op_sel_hi:[1,0]
	v_pk_mul_f32 v[10:11], v[10:11], v[128:129] op_sel_hi:[1,0]
	v_pk_mul_f32 v[8:9], v[8:9], v[128:129] op_sel_hi:[1,0]
	v_pk_mul_f32 v[6:7], v[6:7], v[128:129] op_sel_hi:[1,0]
	v_pk_mul_f32 v[4:5], v[4:5], v[128:129] op_sel_hi:[1,0]
	v_pk_mul_f32 v[2:3], v[2:3], v[128:129] op_sel_hi:[1,0]
	v_pk_mul_f32 v[0:1], v[0:1], v[128:129] op_sel_hi:[1,0]
	v_pk_mul_f32 v[62:63], v[62:63], v[128:129] op_sel_hi:[1,0]
	v_pk_mul_f32 v[60:61], v[60:61], v[128:129] op_sel_hi:[1,0]
	v_pk_mul_f32 v[58:59], v[58:59], v[128:129] op_sel_hi:[1,0]
	v_pk_mul_f32 v[56:57], v[56:57], v[128:129] op_sel_hi:[1,0]
	v_pk_mul_f32 v[54:55], v[54:55], v[128:129] op_sel_hi:[1,0]
	v_pk_mul_f32 v[52:53], v[52:53], v[128:129] op_sel_hi:[1,0]
	v_pk_mul_f32 v[50:51], v[50:51], v[128:129] op_sel_hi:[1,0]
	v_pk_mul_f32 v[48:49], v[48:49], v[128:129] op_sel_hi:[1,0]
	v_pk_mul_f32 v[46:47], v[128:129], v[46:47] op_sel_hi:[0,1]
	v_pk_mul_f32 v[44:45], v[128:129], v[44:45] op_sel_hi:[0,1]
	v_pk_mul_f32 v[42:43], v[128:129], v[42:43] op_sel_hi:[0,1]
	v_pk_mul_f32 v[40:41], v[128:129], v[40:41] op_sel_hi:[0,1]
	v_pk_mul_f32 v[38:39], v[128:129], v[38:39] op_sel_hi:[0,1]
	v_pk_mul_f32 v[36:37], v[128:129], v[36:37] op_sel_hi:[0,1]
	v_pk_mul_f32 v[34:35], v[128:129], v[34:35] op_sel_hi:[0,1]
	v_pk_mul_f32 v[32:33], v[128:129], v[32:33] op_sel_hi:[0,1]
	v_pk_mul_f32 v[30:31], v[128:129], v[30:31] op_sel_hi:[0,1]
	v_pk_mul_f32 v[28:29], v[128:129], v[28:29] op_sel_hi:[0,1]
	v_pk_mul_f32 v[26:27], v[128:129], v[26:27] op_sel_hi:[0,1]
	v_pk_mul_f32 v[24:25], v[128:129], v[24:25] op_sel_hi:[0,1]
	v_pk_mul_f32 v[22:23], v[128:129], v[22:23] op_sel_hi:[0,1]
	v_pk_mul_f32 v[20:21], v[128:129], v[20:21] op_sel_hi:[0,1]
	v_pk_mul_f32 v[18:19], v[128:129], v[18:19] op_sel_hi:[0,1]
	v_pk_mul_f32 v[16:17], v[128:129], v[16:17] op_sel_hi:[0,1]
	s_branch .LBB0_873

.Lgqa_slow_880:
	v_add_u32_e32 v21, 32, v185
	v_and_b32_e32 v17, 0xfffff0, v185
	v_lshlrev_b32_e32 v18, 1, v185
	v_and_b32_e32 v22, 0xfffff0, v21
	v_lshlrev_b32_e32 v23, 1, v21
	v_and_b32_e32 v16, 63, v184
	v_and_or_b32 v17, v18, 8, v17
	v_and_or_b32 v22, v23, 8, v22
	v_lshrrev_b32_e32 v17, 1, v17
	v_lshrrev_b32_e32 v19, 5, v186
	v_lshrrev_b32_e32 v22, 1, v22
	v_lshlrev_b32_e32 v23, 4, v16
	v_lshrrev_b32_e32 v18, 1, v185
	v_or_b32_e32 v17, v17, v19
	v_and_b32_e32 v20, 3, v185
	v_or_b32_e32 v19, v22, v19
	v_lshlrev_b32_e32 v22, 3, v16
	v_and_b32_e32 v23, 0xc0, v23
	v_lshlrev_b32_e32 v16, 1, v16
	v_and_or_b32 v18, v18, 4, v20
	v_lshlrev_b32_e32 v20, 1, v186
	v_and_or_b32 v23, v22, 24, v23
	v_and_b32_e32 v16, 32, v16
	v_and_b32_e32 v22, 0x100, v22
	v_lshlrev_b32_e32 v17, 9, v17
	v_lshlrev_b32_e32 v18, 6, v18
	v_or3_b32 v114, v23, v16, v22
	v_and_b32_e32 v16, 48, v20
	v_or3_b32 v17, v17, v18, v16
	v_add_u32_e32 v212, 0, v17
	v_lshrrev_b32_e32 v22, 3, v212
	v_xor_b32_e32 v22, v22, v212
	v_and_b32_e32 v22, 0x100, v22
	v_lshl_or_b32 v23, v22, 3, v22
	v_xor_b32_e32 v212, v212, v23
	v_lshlrev_b32_e32 v19, 9, v19
	v_cvt_pk_bf16_f32 v138, v176, v177
	v_cvt_pk_bf16_f32 v139, v170, v171
	v_cvt_pk_bf16_f32 v140, v164, v165
	v_cvt_pk_bf16_f32 v141, v144, v145
	v_cvt_pk_bf16_f32 v154, v142, v143
	v_cvt_pk_bf16_f32 v155, v136, v137
	v_cvt_pk_bf16_f32 v156, v134, v135
	v_cvt_pk_bf16_f32 v157, v132, v133
	v_cvt_pk_bf16_f32 v158, v130, v131
	v_cvt_pk_bf16_f32 v159, v126, v127
	v_cvt_pk_bf16_f32 v160, v124, v125
	v_cvt_pk_bf16_f32 v161, v122, v123
	v_cvt_pk_bf16_f32 v150, v120, v121
	v_cvt_pk_bf16_f32 v151, v118, v119
	v_cvt_pk_bf16_f32 v152, v116, v117
	v_cvt_pk_bf16_f32 v153, v112, v113
	v_cvt_pk_bf16_f32 v146, v108, v109
	v_cvt_pk_bf16_f32 v147, v110, v111
	v_cvt_pk_bf16_f32 v148, v104, v105
	v_cvt_pk_bf16_f32 v149, v106, v107
	v_cvt_pk_bf16_f32 v142, v100, v101
	v_cvt_pk_bf16_f32 v143, v102, v103
	v_cvt_pk_bf16_f32 v144, v96, v97
	v_cvt_pk_bf16_f32 v145, v98, v99
	v_cvt_pk_bf16_f32 v134, v92, v93
	v_cvt_pk_bf16_f32 v135, v94, v95
	v_cvt_pk_bf16_f32 v136, v88, v89
	v_cvt_pk_bf16_f32 v137, v90, v91
	v_cvt_pk_bf16_f32 v130, v84, v85
	v_cvt_pk_bf16_f32 v131, v86, v87
	v_cvt_pk_bf16_f32 v132, v80, v81
	v_cvt_pk_bf16_f32 v133, v82, v83
	s_waitcnt vmcnt(0)
	ds_write_b128 v212, v[8:11]
	v_lshlrev_b32_e32 v8, 8, v185
	v_and_b32_e32 v9, 0x70, v184
	v_or3_b32 v16, v19, v18, v16
	v_bitop3_b32 v8, v20, v8, v9 bitop3:0xde
	v_add_u32_e32 v213, 0, v16
	v_lshrrev_b32_e32 v16, 3, v213
	v_xor_b32_e32 v16, v16, v213
	v_and_b32_e32 v16, 0x100, v16
	v_lshl_or_b32 v17, v16, 3, v16
	v_xor_b32_e32 v213, v213, v17
	v_add_u32_e32 v214, 0, v8
	ds_write_b128 v213, v[12:15]
	ds_write_b128 v214, v[4:7] offset:32768
	v_lshlrev_b32_e32 v4, 8, v21
	v_bitop3_b32 v4, v20, v4, v9 bitop3:0xde
	v_add_u32_e32 v215, 0, v4
	ds_write_b128 v215, v[0:3] offset:32768
	v_lshlrev_b32_e32 v0, 4, v163
	v_lshlrev_b32_e32 v56, 8, v163
	v_and_b32_e32 v57, 0x70, v0
	v_bitop3_b32 v0, v162, v56, v57 bitop3:0xde
	v_add_u32_e32 v216, 0, v0
	s_waitcnt lgkmcnt(0)
	s_barrier
	ds_read_b128 v[16:19], v216 offset:32768
	ds_read_b128 v[20:23], v216 offset:40960
	s_waitcnt lgkmcnt(1)
	v_mfma_f32_32x32x16_bf16 v[32:47], v[16:19], v[138:141], 0
	v_or_b32_e32 v48, 32, v162
	v_bitop3_b32 v48, v48, v56, v57 bitop3:0xde
	v_add_u32_e32 v218, 0, v48
	ds_read_b128 v[48:51], v218 offset:32768
	ds_read_b128 v[52:55], v218 offset:40960
	s_cmp_lg_u32 0, -1
	s_cselect_b32 s53, 0, 0
	s_add_u32 s16, s10, s96
	s_waitcnt lgkmcnt(2)
	v_mfma_f32_32x32x16_bf16 v[16:31], v[20:23], v[138:141], 0
	s_addc_u32 s17, s11, s97
	v_mov_b32_e32 v199, v129
	s_add_u32 s18, s8, s96
	s_addc_u32 s19, s9, s97
	v_lshl_add_u64 v[60:61], s[18:19], 0, v[198:199]
	s_add_u32 s2, s16, s96
	s_addc_u32 s3, s17, s97
	s_waitcnt lgkmcnt(1)
	v_mfma_f32_32x32x16_bf16 v[32:47], v[48:51], v[154:157], v[32:47]
	v_or_b32_e32 v48, 64, v162
	v_bitop3_b32 v48, v48, v56, v57 bitop3:0xde
	v_add_u32_e32 v219, 0, v48
	v_lshl_add_u64 v[64:65], s[2:3], 0, v[128:129]
	s_mov_b32 s72, s73
	s_mov_b32 s74, s73
	s_mov_b32 s75, s73
	s_waitcnt lgkmcnt(0)
	v_mfma_f32_32x32x16_bf16 v[16:31], v[52:55], v[154:157], v[16:31]
	ds_read_b128 v[48:51], v219 offset:32768
	ds_read_b128 v[52:55], v219 offset:40960
	s_mov_b32 s76, s73
	s_mov_b32 s77, s73
	s_mov_b32 s78, s73
	s_mov_b32 s79, s73
	s_mov_b32 s80, s73
	s_mov_b32 s81, s73
	s_waitcnt lgkmcnt(1)
	v_mfma_f32_32x32x16_bf16 v[32:47], v[48:51], v[158:161], v[32:47]
	v_or_b32_e32 v48, 0x60, v162
	v_bitop3_b32 v48, v48, v56, v57 bitop3:0xde
	v_add_u32_e32 v220, 0, v48
	s_mov_b32 s82, s73
	s_mov_b32 s83, s73
	s_mov_b32 s84, s73
	s_mov_b32 s85, s73
	s_waitcnt lgkmcnt(0)
	v_mfma_f32_32x32x16_bf16 v[16:31], v[52:55], v[158:161], v[16:31]
	ds_read_b128 v[48:51], v220 offset:32768
	ds_read_b128 v[52:55], v220 offset:40960
	s_mov_b32 s86, s73
	s_mov_b32 s87, s73
	v_mov_b64_e32 v[0:1], s[72:73]
	v_mov_b64_e32 v[14:15], s[86:87]
	v_add_u32_e32 v209, s53, v114
	v_mov_b64_e32 v[2:3], s[74:75]
	s_waitcnt lgkmcnt(1)
	v_mfma_f32_32x32x16_bf16 v[32:47], v[48:51], v[150:153], v[32:47]
	v_or_b32_e32 v48, 0x80, v162
	v_bitop3_b32 v48, v48, v56, v57 bitop3:0xde
	v_add_u32_e32 v221, 0, v48
	v_mov_b64_e32 v[4:5], s[76:77]
	v_mov_b64_e32 v[6:7], s[78:79]
	v_mov_b64_e32 v[8:9], s[80:81]
	v_mov_b64_e32 v[10:11], s[82:83]
	s_waitcnt lgkmcnt(0)
	v_mfma_f32_32x32x16_bf16 v[16:31], v[52:55], v[150:153], v[16:31]
	ds_read_b128 v[48:51], v221 offset:32768
	ds_read_b128 v[52:55], v221 offset:40960
	v_mov_b64_e32 v[12:13], s[84:85]
	s_mov_b32 s39, 4
	v_mov_b32_e32 v217, 0
	v_readlane_b32 s80, v255, 48
	s_movk_i32 s79, 0xff
	s_movk_i32 s84, 0xffe0
	s_waitcnt lgkmcnt(1)
	v_mfma_f32_32x32x16_bf16 v[32:47], v[48:51], v[146:149], v[32:47]
	v_or_b32_e32 v48, 0xa0, v162
	v_bitop3_b32 v48, v48, v56, v57 bitop3:0xde
	v_add_u32_e32 v222, 0, v48
	s_waitcnt lgkmcnt(0)
	v_mfma_f32_32x32x16_bf16 v[16:31], v[52:55], v[146:149], v[16:31]
	ds_read_b128 v[48:51], v222 offset:32768
	ds_read_b128 v[52:55], v222 offset:40960
	s_waitcnt lgkmcnt(1)
	v_mfma_f32_32x32x16_bf16 v[32:47], v[48:51], v[142:145], v[32:47]
	v_or_b32_e32 v48, 0xc0, v162
	v_bitop3_b32 v48, v48, v56, v57 bitop3:0xde
	v_add_u32_e32 v224, 0, v48
	s_waitcnt lgkmcnt(0)
	v_mfma_f32_32x32x16_bf16 v[16:31], v[52:55], v[142:145], v[16:31]
	ds_read_b128 v[48:51], v224 offset:32768
	ds_read_b128 v[52:55], v224 offset:40960
	s_waitcnt lgkmcnt(1)
	v_mfma_f32_32x32x16_bf16 v[32:47], v[48:51], v[134:137], v[32:47]
	v_or_b32_e32 v48, 0xe0, v162
	v_bitop3_b32 v48, v48, v56, v57 bitop3:0xde
	v_add_u32_e32 v223, 0, v48
	v_lshl_add_u64 v[56:57], s[18:19], 0, v[128:129]
	s_waitcnt lgkmcnt(0)
	v_mfma_f32_32x32x16_bf16 v[16:31], v[52:55], v[134:137], v[16:31]
	ds_read_b128 v[48:51], v223 offset:32768
	ds_read_b128 v[52:55], v223 offset:40960
	global_load_dwordx4 v[56:59], v[56:57], off
	s_nop 0
	global_load_dwordx4 v[60:63], v[60:61], off
	s_nop 0
	global_load_dwordx4 v[162:165], v[64:65], off
	v_lshl_add_u64 v[64:65], s[2:3], 0, v[198:199]
	s_waitcnt lgkmcnt(1)
	v_mfma_f32_32x32x16_bf16 v[32:47], v[48:51], v[130:133], v[32:47]
	global_load_dwordx4 v[166:169], v[64:65], off
	s_waitcnt lgkmcnt(0)
	v_mfma_f32_32x32x16_bf16 v[16:31], v[52:55], v[130:133], v[16:31]
	s_nop 8
	v_max_f32_e32 v48, v33, v33
	v_max_f32_e32 v49, v32, v32
	v_max_f32_e32 v48, v49, v48
	v_max_f32_e32 v49, v41, v41
	v_max_f32_e32 v50, v40, v40
	v_max_f32_e32 v49, v50, v49
	v_max3_f32 v48, v48, v34, v35
	v_max_f32_e32 v50, v25, v25
	v_max_f32_e32 v51, v24, v24
	v_max_f32_e32 v50, v51, v50
	v_max3_f32 v51, v16, v17, v18
	v_max3_f32 v50, v50, v26, v27
	v_max3_f32 v49, v49, v42, v43
	v_max3_f32 v51, v51, v19, v20
	v_max3_f32 v50, v50, v28, v29
	v_max3_f32 v48, v48, v36, v37
	v_max3_f32 v49, v49, v44, v45
	v_max3_f32 v51, v51, v21, v22
	v_max3_f32 v50, v50, v30, v31
	v_max3_f32 v48, v48, v38, v39
	v_max3_f32 v49, v49, v46, v47
	v_max3_f32 v50, v51, v23, v50
	v_max3_f32 v48, v48, v49, v50
	v_mov_b32_e32 v49, v48
	s_nop 1
	v_permlane32_swap_b32_e32 v48, v49
	v_max_f32_e32 v49, v49, v49
	v_max_f32_e32 v48, v48, v48
	v_max_f32_e32 v66, v48, v49
	v_add_f32_e32 v48, 0x7149f2ca, v66
	v_cmp_ge_f32_e32 vcc, s31, v48
	v_lshl_add_u64 v[48:49], s[16:17], 0, v[128:129]
	global_load_dwordx4 v[48:51], v[48:49], off
	v_lshl_add_u64 v[52:53], s[16:17], 0, v[198:199]
	global_load_dwordx4 v[52:55], v[52:53], off
	s_add_u32 s16, s18, s96
	s_addc_u32 s17, s19, s97
	v_lshl_add_u64 v[64:65], s[16:17], 0, v[128:129]
	global_load_dwordx4 v[170:173], v[64:65], off
	v_lshl_add_u64 v[64:65], s[16:17], 0, v[198:199]
	global_load_dwordx4 v[174:177], v[64:65], off
	s_and_b64 s[2:3], s[14:15], exec
	s_cselect_b32 s14, 3, 35
	s_cmp_eq_u64 vcc, exec
	s_waitcnt vmcnt(4)
	s_waitcnt vmcnt(3)
	ds_write_b128 v212, v[48:51] offset:16384
	s_waitcnt vmcnt(2)
	ds_write_b128 v213, v[52:55] offset:16384
	ds_write_b128 v214, v[56:59] offset:49152
	ds_write_b128 v215, v[60:63] offset:49152
	s_cselect_b64 vcc, -1, 0
	v_max_f32_e32 v49, 0xf149f2ca, v66
	v_cndmask_b32_e32 v226, v49, v230, vcc
	v_mul_f32_e32 v48, 0xbe0293ee, v226
	v_fmamk_f32 v32, v32, 0x3e0293ee, v48
	v_exp_f32_e32 v64, v32
	v_fmamk_f32 v32, v33, 0x3e0293ee, v48
	v_exp_f32_e32 v65, v32
	v_fmamk_f32 v32, v34, 0x3e0293ee, v48
	v_exp_f32_e32 v66, v32
	v_fmamk_f32 v32, v35, 0x3e0293ee, v48
	v_exp_f32_e32 v67, v32
	v_fmamk_f32 v32, v36, 0x3e0293ee, v48
	v_exp_f32_e32 v68, v32
	v_fmamk_f32 v32, v37, 0x3e0293ee, v48
	v_exp_f32_e32 v69, v32
	v_fmamk_f32 v32, v38, 0x3e0293ee, v48
	v_exp_f32_e32 v70, v32
	v_fmamk_f32 v32, v39, 0x3e0293ee, v48
	v_exp_f32_e32 v71, v32
	v_fmamk_f32 v32, v40, 0x3e0293ee, v48
	v_exp_f32_e32 v72, v32
	v_fmamk_f32 v32, v41, 0x3e0293ee, v48
	v_exp_f32_e32 v73, v32
	v_fmamk_f32 v32, v42, 0x3e0293ee, v48
	v_exp_f32_e32 v74, v32
	v_fmamk_f32 v32, v43, 0x3e0293ee, v48
	v_pk_fma_f32 v[80:81], v[16:17], s[52:53], v[48:49] op_sel_hi:[1,0,0]
	v_sub_f32_e32 v16, 0xf149f2ca, v49
	v_exp_f32_e32 v75, v32
	v_fmamk_f32 v32, v44, 0x3e0293ee, v48
	v_mul_f32_e32 v16, 0x3e0293ee, v16
	v_exp_f32_e32 v76, v32
	v_fmamk_f32 v32, v45, 0x3e0293ee, v48
	v_exp_f32_e32 v16, v16
	v_exp_f32_e32 v77, v32
	v_fmamk_f32 v32, v46, 0x3e0293ee, v48
	v_exp_f32_e32 v78, v32
	v_fmamk_f32 v32, v47, 0x3e0293ee, v48
	v_exp_f32_e32 v79, v32
	v_pk_fma_f32 v[82:83], v[18:19], s[52:53], v[48:49] op_sel_hi:[1,0,0]
	v_cndmask_b32_e64 v225, v16, 1.0, vcc
	v_lshl_add_u64 v[16:17], s[12:13], 0, v[128:129]
	v_lshl_add_u64 v[18:19], s[12:13], 0, v[198:199]
	v_pk_fma_f32 v[94:95], v[30:31], s[52:53], v[48:49] op_sel_hi:[1,0,0]
	v_pk_fma_f32 v[92:93], v[28:29], s[52:53], v[48:49] op_sel_hi:[1,0,0]
	v_pk_fma_f32 v[90:91], v[26:27], s[52:53], v[48:49] op_sel_hi:[1,0,0]
	v_pk_fma_f32 v[88:89], v[24:25], s[52:53], v[48:49] op_sel_hi:[1,0,0]
	v_pk_fma_f32 v[86:87], v[22:23], s[52:53], v[48:49] op_sel_hi:[1,0,0]
	v_pk_fma_f32 v[84:85], v[20:21], s[52:53], v[48:49] op_sel_hi:[1,0,0]
	s_addk_i32 s53, 0x4000
	v_lshl_add_u64 v[200:201], s[64:65], 0, v[16:17]
	v_lshl_add_u64 v[202:203], s[64:65], 0, v[18:19]
	v_lshl_add_u64 v[204:205], s[66:67], 0, v[16:17]
	v_lshl_add_u64 v[206:207], s[66:67], 0, v[18:19]
	v_mov_b64_e32 v[62:63], v[14:15]
	v_mov_b64_e32 v[46:47], v[14:15]
	v_mov_b64_e32 v[30:31], v[14:15]
	v_add_u32_e32 v211, s53, v114
	v_mov_b64_e32 v[60:61], v[12:13]
	v_mov_b64_e32 v[58:59], v[10:11]
	v_mov_b64_e32 v[56:57], v[8:9]
	v_mov_b64_e32 v[54:55], v[6:7]
	v_mov_b64_e32 v[52:53], v[4:5]
	v_mov_b64_e32 v[50:51], v[2:3]
	v_mov_b64_e32 v[48:49], v[0:1]
	v_mov_b64_e32 v[44:45], v[12:13]
	v_mov_b64_e32 v[42:43], v[10:11]
	v_mov_b64_e32 v[40:41], v[8:9]
	v_mov_b64_e32 v[38:39], v[6:7]
	v_mov_b64_e32 v[36:37], v[4:5]
	v_mov_b64_e32 v[34:35], v[2:3]
	v_mov_b64_e32 v[32:33], v[0:1]
	v_mov_b64_e32 v[28:29], v[12:13]
	v_mov_b64_e32 v[26:27], v[10:11]
	v_mov_b64_e32 v[24:25], v[8:9]
	v_mov_b64_e32 v[22:23], v[6:7]
	v_mov_b64_e32 v[20:21], v[4:5]
	v_mov_b64_e32 v[18:19], v[2:3]
	v_mov_b64_e32 v[16:17], v[0:1]
	s_mov_b32 s53, 0x38e38e39
	s_waitcnt lgkmcnt(0)
	s_barrier
.Lgqa_slow_881:
	ds_read_b128 v[96:99], v216 offset:49152
	ds_read_b128 v[100:103], v216 offset:57344
	ds_read_b128 v[178:181], v218 offset:49152
	ds_read_b128 v[182:185], v218 offset:57344
	v_exp_f32_e32 v80, v80
	v_exp_f32_e32 v81, v81
	s_waitcnt lgkmcnt(3)
	v_mfma_f32_32x32x16_bf16 v[112:127], v[96:99], v[138:141], 0
	v_exp_f32_e32 v82, v82
	v_exp_f32_e32 v83, v83
	v_exp_f32_e32 v84, v84
	v_exp_f32_e32 v92, v92
	v_exp_f32_e32 v85, v85
	v_exp_f32_e32 v93, v93
	v_exp_f32_e32 v86, v86
	s_waitcnt lgkmcnt(2)
	v_mfma_f32_32x32x16_bf16 v[96:111], v[100:103], v[138:141], 0
	v_exp_f32_e32 v94, v94
	v_exp_f32_e32 v87, v87
	v_exp_f32_e32 v95, v95
	s_waitcnt lgkmcnt(1)
	v_mfma_f32_32x32x16_bf16 v[112:127], v[178:181], v[154:157], v[112:127]
	s_waitcnt lgkmcnt(0)
	v_mfma_f32_32x32x16_bf16 v[96:111], v[182:185], v[154:157], v[96:111]
	ds_read_b128 v[178:181], v219 offset:49152
	ds_read_b128 v[182:185], v219 offset:57344
	s_waitcnt lgkmcnt(1)
	v_mfma_f32_32x32x16_bf16 v[112:127], v[178:181], v[158:161], v[112:127]
	s_waitcnt lgkmcnt(0)
	v_mfma_f32_32x32x16_bf16 v[96:111], v[182:185], v[158:161], v[96:111]
	ds_read_b128 v[178:181], v220 offset:49152
	ds_read_b128 v[182:185], v220 offset:57344
	s_waitcnt lgkmcnt(1)
	v_mfma_f32_32x32x16_bf16 v[112:127], v[178:181], v[150:153], v[112:127]
	s_waitcnt lgkmcnt(0)
	v_mfma_f32_32x32x16_bf16 v[96:111], v[182:185], v[150:153], v[96:111]
	ds_read_b128 v[178:181], v221 offset:49152
	ds_read_b128 v[182:185], v221 offset:57344
	s_waitcnt lgkmcnt(1)
	v_mfma_f32_32x32x16_bf16 v[112:127], v[178:181], v[146:149], v[112:127]
	s_waitcnt lgkmcnt(0)
	v_mfma_f32_32x32x16_bf16 v[96:111], v[182:185], v[146:149], v[96:111]
	ds_read_b128 v[178:181], v222 offset:49152
	ds_read_b128 v[182:185], v222 offset:57344
	s_waitcnt lgkmcnt(1)
	v_mfma_f32_32x32x16_bf16 v[112:127], v[178:181], v[142:145], v[112:127]
	s_waitcnt lgkmcnt(0)
	v_mfma_f32_32x32x16_bf16 v[96:111], v[182:185], v[142:145], v[96:111]
	ds_read_b128 v[178:181], v224 offset:49152
	ds_read_b128 v[182:185], v224 offset:57344
	s_waitcnt lgkmcnt(1)
	v_mfma_f32_32x32x16_bf16 v[112:127], v[178:181], v[134:137], v[112:127]
	s_waitcnt lgkmcnt(0)
	v_mfma_f32_32x32x16_bf16 v[96:111], v[182:185], v[134:137], v[96:111]
	ds_read_b128 v[178:181], v223 offset:49152
	ds_read_b128 v[182:185], v223 offset:57344
	s_waitcnt lgkmcnt(1)
	v_mfma_f32_32x32x16_bf16 v[112:127], v[178:181], v[130:133], v[112:127]
	v_exp_f32_e32 v178, v88
	v_exp_f32_e32 v179, v89
	v_exp_f32_e32 v180, v90
	v_exp_f32_e32 v181, v91
	v_add_f32_e32 v88, v64, v65
	v_add_f32_e32 v89, v72, v73
	v_add_f32_e32 v90, v80, v81
	v_add_f32_e32 v91, v178, v179
	v_add_f32_e32 v88, v66, v88
	v_add_f32_e32 v89, v74, v89
	v_add_f32_e32 v90, v82, v90
	v_add_f32_e32 v91, v180, v91
	v_add_f32_e32 v88, v67, v88
	v_add_f32_e32 v89, v75, v89
	v_add_f32_e32 v90, v83, v90
	v_add_f32_e32 v91, v181, v91
	v_add_f32_e32 v88, v68, v88
	v_add_f32_e32 v89, v76, v89
	v_add_f32_e32 v90, v84, v90
	v_add_f32_e32 v91, v92, v91
	v_add_f32_e32 v88, v69, v88
	v_add_f32_e32 v89, v77, v89
	v_add_f32_e32 v90, v85, v90
	v_add_f32_e32 v91, v93, v91
	v_add_f32_e32 v88, v70, v88
	v_add_f32_e32 v89, v78, v89
	v_add_f32_e32 v90, v86, v90
	v_add_f32_e32 v91, v94, v91
	v_add_f32_e32 v88, v71, v88
	v_add_f32_e32 v89, v79, v89
	v_add_f32_e32 v90, v87, v90
	v_add_f32_e32 v91, v95, v91
	v_add_f32_e32 v88, v89, v88
	v_add_f32_e32 v89, v91, v90
	v_add_f32_e32 v227, v88, v89
	v_mov_b32_e32 v228, v227
	v_cvt_pk_bf16_f32 v88, v64, v65
	v_cvt_pk_bf16_f32 v89, v66, v67
	v_cvt_pk_bf16_f32 v90, v68, v69
	v_cvt_pk_bf16_f32 v91, v70, v71
	s_nop 1
	v_permlane32_swap_b32_e32 v227, v228
	v_cvt_pk_bf16_f32 v72, v72, v73
	v_cvt_pk_bf16_f32 v73, v74, v75
	v_cvt_pk_bf16_f32 v74, v76, v77
	v_cvt_pk_bf16_f32 v75, v78, v79
	v_cvt_pk_bf16_f32 v64, v80, v81
	v_cvt_pk_bf16_f32 v65, v82, v83
	v_cvt_pk_bf16_f32 v66, v84, v85
	v_cvt_pk_bf16_f32 v67, v86, v87
	v_cvt_pk_bf16_f32 v68, v178, v179
	v_cvt_pk_bf16_f32 v69, v180, v181
	v_cvt_pk_bf16_f32 v70, v92, v93
	v_cvt_pk_bf16_f32 v71, v94, v95
	s_waitcnt lgkmcnt(0)
	v_mfma_f32_32x32x16_bf16 v[96:111], v[182:185], v[130:133], v[96:111]
	v_lshl_add_u64 v[76:77], v[200:201], 0, s[92:93]
	global_load_dwordx4 v[178:181], v[76:77], off
	v_lshl_add_u64 v[76:77], v[202:203], 0, s[92:93]
	global_load_dwordx4 v[182:185], v[76:77], off
	v_lshl_add_u64 v[76:77], v[204:205], 0, s[92:93]
	global_load_dwordx4 v[186:189], v[76:77], off
	v_lshl_add_u64 v[76:77], v[206:207], 0, s[92:93]
	global_load_dwordx4 v[190:193], v[76:77], off
	ds_read_b64_tr_b16 v[76:77], v209 offset:0
	ds_read_b64_tr_b16 v[78:79], v209 offset:0x800
	ds_read_b64_tr_b16 v[80:81], v209 offset:0x1000
	ds_read_b64_tr_b16 v[82:83], v209 offset:0x1800
	ds_read_b64_tr_b16 v[84:85], v209 offset:0x2000
	ds_read_b64_tr_b16 v[86:87], v209 offset:0x2800
	ds_read_b64_tr_b16 v[92:93], v209 offset:0x3000
	ds_read_b64_tr_b16 v[94:95], v209 offset:0x3800
	s_waitcnt lgkmcnt(0)
	s_nop 0
	v_mfma_f32_32x32x16_bf16 v[0:15], v[76:79], v[88:91], v[0:15]
	v_max_f32_e32 v76, v97, v97
	v_max_f32_e32 v77, v96, v96
	v_max_f32_e32 v76, v77, v76
	v_max3_f32 v77, v112, v113, v114
	v_max3_f32 v76, v76, v98, v99
	v_max3_f32 v77, v77, v115, v116
	v_max3_f32 v76, v76, v100, v101
	v_mfma_f32_32x32x16_bf16 v[0:15], v[80:83], v[72:75], v[0:15]
	v_max3_f32 v77, v77, v117, v118
	v_max3_f32 v76, v76, v102, v103
	v_max3_f32 v77, v77, v119, v120
	v_max3_f32 v76, v76, v104, v105
	v_max3_f32 v77, v77, v121, v122
	v_max3_f32 v76, v76, v106, v107
	v_max3_f32 v77, v77, v123, v124
	v_mfma_f32_32x32x16_bf16 v[0:15], v[84:87], v[64:67], v[0:15]
	v_max3_f32 v76, v76, v108, v109
	v_max3_f32 v77, v77, v125, v126
	v_max3_f32 v76, v76, v110, v111
	v_max3_f32 v194, v77, v127, v76
	ds_read_b64_tr_b16 v[76:77], v209 offset:0x200
	ds_read_b64_tr_b16 v[78:79], v209 offset:0xa00
	ds_read_b64_tr_b16 v[80:81], v209 offset:0x1200
	v_mfma_f32_32x32x16_bf16 v[0:15], v[92:95], v[68:71], v[0:15]
	ds_read_b64_tr_b16 v[82:83], v209 offset:0x1a00
	ds_read_b64_tr_b16 v[84:85], v209 offset:0x2200
	ds_read_b64_tr_b16 v[86:87], v209 offset:0x2a00
	ds_read_b64_tr_b16 v[92:93], v209 offset:0x3200
	ds_read_b64_tr_b16 v[94:95], v209 offset:0x3a00
	s_waitcnt lgkmcnt(0)
	v_mfma_f32_32x32x16_bf16 v[48:63], v[76:79], v[88:91], v[48:63]
	v_mov_b32_e32 v76, v194
	s_nop 1
	v_permlane32_swap_b32_e32 v194, v76
	v_max_f32_e32 v76, v76, v76
	v_max_f32_e32 v77, v194, v194
	v_max_f32_e32 v76, v77, v76
	v_sub_f32_e32 v77, v76, v226
	v_mfma_f32_32x32x16_bf16 v[48:63], v[80:83], v[72:75], v[48:63]
	v_cmp_ge_f32_e32 vcc, s31, v77
	v_max_f32_e32 v77, v226, v226
	v_max_f32_e32 v76, v77, v76
	v_sub_f32_e32 v77, v226, v76
	v_mul_f32_e32 v77, 0x3e0293ee, v77
	v_exp_f32_e32 v77, v77
	s_cmp_eq_u64 vcc, exec
	v_mfma_f32_32x32x16_bf16 v[48:63], v[84:87], v[64:67], v[48:63]
	s_cselect_b64 vcc, -1, 0
	v_cndmask_b32_e64 v210, v77, 1.0, vcc
	v_cndmask_b32_e32 v226, v76, v226, vcc
	ds_read_b64_tr_b16 v[76:77], v209 offset:0x400
	ds_read_b64_tr_b16 v[78:79], v209 offset:0xc00
	ds_read_b64_tr_b16 v[80:81], v209 offset:0x1400
	ds_read_b64_tr_b16 v[82:83], v209 offset:0x1c00
	v_mfma_f32_32x32x16_bf16 v[48:63], v[92:95], v[68:71], v[48:63]
	ds_read_b64_tr_b16 v[84:85], v209 offset:0x2400
	ds_read_b64_tr_b16 v[86:87], v209 offset:0x2c00
	ds_read_b64_tr_b16 v[92:93], v209 offset:0x3400
	ds_read_b64_tr_b16 v[94:95], v209 offset:0x3c00
	s_waitcnt lgkmcnt(0)
	v_mul_f32_e32 v208, 0xbe0293ee, v226
	v_fmamk_f32 v194, v112, 0x3e0293ee, v208
	v_fmamk_f32 v195, v113, 0x3e0293ee, v208
	v_fmamk_f32 v196, v114, 0x3e0293ee, v208
	v_fmamk_f32 v197, v115, 0x3e0293ee, v208
	v_fmamk_f32 v229, v116, 0x3e0293ee, v208
	v_fmamk_f32 v233, v117, 0x3e0293ee, v208
	v_fmamk_f32 v234, v118, 0x3e0293ee, v208
	v_fmamk_f32 v235, v119, 0x3e0293ee, v208
	v_fmamk_f32 v236, v120, 0x3e0293ee, v208
	v_fmamk_f32 v237, v121, 0x3e0293ee, v208
	v_fmamk_f32 v238, v122, 0x3e0293ee, v208
	v_fmamk_f32 v239, v123, 0x3e0293ee, v208
	v_fmamk_f32 v240, v124, 0x3e0293ee, v208
	v_fmamk_f32 v241, v125, 0x3e0293ee, v208
	v_fmamk_f32 v242, v126, 0x3e0293ee, v208
	v_fmamk_f32 v243, v127, 0x3e0293ee, v208
	v_mfma_f32_32x32x16_bf16 v[32:47], v[76:79], v[88:91], v[32:47]
	ds_read_b64_tr_b16 v[76:77], v209 offset:0x600
	ds_read_b64_tr_b16 v[78:79], v209 offset:0xe00
	v_fma_f32 v112, v96, s52, v208
	v_fma_f32 v113, v97, s52, v208
	v_fma_f32 v114, v98, s52, v208
	v_fma_f32 v115, v99, s52, v208
	v_fma_f32 v116, v100, s52, v208
	v_fma_f32 v117, v101, s52, v208
	v_pk_fma_f32 v[118:119], v[102:103], s[52:53], v[208:209] op_sel_hi:[1,0,0]
	v_pk_fma_f32 v[126:127], v[110:111], s[52:53], v[208:209] op_sel_hi:[1,0,0]
	v_mfma_f32_32x32x16_bf16 v[32:47], v[80:83], v[72:75], v[32:47]
	v_exp_f32_e32 v80, v194
	v_exp_f32_e32 v81, v195
	v_exp_f32_e32 v82, v196
	v_exp_f32_e32 v83, v197
	v_pk_fma_f32 v[124:125], v[108:109], s[52:53], v[208:209] op_sel_hi:[1,0,0]
	v_pk_fma_f32 v[122:123], v[106:107], s[52:53], v[208:209] op_sel_hi:[1,0,0]
	v_pk_fma_f32 v[120:121], v[104:105], s[52:53], v[208:209] op_sel_hi:[1,0,0]
	v_mfma_f32_32x32x16_bf16 v[32:47], v[84:87], v[64:67], v[32:47]
	v_exp_f32_e32 v84, v229
	v_exp_f32_e32 v85, v233
	v_exp_f32_e32 v86, v234
	v_exp_f32_e32 v87, v235
	v_mfma_f32_32x32x16_bf16 v[32:47], v[92:95], v[68:71], v[32:47]
	ds_read_b64_tr_b16 v[92:93], v209 offset:0x1600
	ds_read_b64_tr_b16 v[94:95], v209 offset:0x1e00
	ds_read_b64_tr_b16 v[96:97], v209 offset:0x2600
	ds_read_b64_tr_b16 v[98:99], v209 offset:0x2e00
	ds_read_b64_tr_b16 v[100:101], v209 offset:0x3600
	ds_read_b64_tr_b16 v[102:103], v209 offset:0x3e00
	s_waitcnt lgkmcnt(0)
	v_mfma_f32_32x32x16_bf16 v[16:31], v[76:79], v[88:91], v[16:31]
	v_exp_f32_e32 v88, v236
	v_exp_f32_e32 v89, v237
	v_exp_f32_e32 v90, v238
	v_exp_f32_e32 v91, v239
	v_cmp_gt_f32_e32 vcc, 1.0, v210
	v_mfma_f32_32x32x16_bf16 v[16:31], v[92:95], v[72:75], v[16:31]
	v_exp_f32_e32 v92, v240
	v_exp_f32_e32 v93, v241
	v_exp_f32_e32 v94, v242
	v_exp_f32_e32 v95, v243
	s_barrier
	v_mfma_f32_32x32x16_bf16 v[16:31], v[96:99], v[64:67], v[16:31]
	s_waitcnt vmcnt(4)
	s_waitcnt vmcnt(7)
	ds_write_b128 v212, v[162:165]
	s_waitcnt vmcnt(6)
	ds_write_b128 v213, v[166:169]
	s_waitcnt vmcnt(5)
	ds_write_b128 v214, v[170:173] offset:32768
	s_waitcnt vmcnt(4)
	ds_write_b128 v215, v[174:177] offset:32768
	v_mfma_f32_32x32x16_bf16 v[16:31], v[100:103], v[68:71], v[16:31]
	s_cbranch_vccz .Lgqa_slow_883
	v_pk_mul_f32 v[14:15], v[14:15], v[210:211] op_sel_hi:[1,0]
	v_pk_mul_f32 v[12:13], v[12:13], v[210:211] op_sel_hi:[1,0]
	v_pk_mul_f32 v[10:11], v[10:11], v[210:211] op_sel_hi:[1,0]
	v_pk_mul_f32 v[8:9], v[8:9], v[210:211] op_sel_hi:[1,0]
	v_pk_mul_f32 v[6:7], v[6:7], v[210:211] op_sel_hi:[1,0]
	v_pk_mul_f32 v[4:5], v[4:5], v[210:211] op_sel_hi:[1,0]
	v_pk_mul_f32 v[2:3], v[2:3], v[210:211] op_sel_hi:[1,0]
	v_pk_mul_f32 v[0:1], v[0:1], v[210:211] op_sel_hi:[1,0]
	v_pk_mul_f32 v[62:63], v[62:63], v[210:211] op_sel_hi:[1,0]
	v_pk_mul_f32 v[60:61], v[60:61], v[210:211] op_sel_hi:[1,0]
	v_pk_mul_f32 v[58:59], v[58:59], v[210:211] op_sel_hi:[1,0]
	v_pk_mul_f32 v[56:57], v[56:57], v[210:211] op_sel_hi:[1,0]
	v_pk_mul_f32 v[54:55], v[54:55], v[210:211] op_sel_hi:[1,0]
	v_pk_mul_f32 v[52:53], v[52:53], v[210:211] op_sel_hi:[1,0]
	v_pk_mul_f32 v[50:51], v[50:51], v[210:211] op_sel_hi:[1,0]
	v_pk_mul_f32 v[48:49], v[48:49], v[210:211] op_sel_hi:[1,0]
	v_pk_mul_f32 v[46:47], v[210:211], v[46:47] op_sel_hi:[0,1]
	v_pk_mul_f32 v[44:45], v[210:211], v[44:45] op_sel_hi:[0,1]
	v_pk_mul_f32 v[42:43], v[210:211], v[42:43] op_sel_hi:[0,1]
	v_pk_mul_f32 v[40:41], v[210:211], v[40:41] op_sel_hi:[0,1]
	v_pk_mul_f32 v[38:39], v[210:211], v[38:39] op_sel_hi:[0,1]
	v_pk_mul_f32 v[36:37], v[210:211], v[36:37] op_sel_hi:[0,1]
	v_pk_mul_f32 v[34:35], v[210:211], v[34:35] op_sel_hi:[0,1]
	v_pk_mul_f32 v[32:33], v[210:211], v[32:33] op_sel_hi:[0,1]
	v_pk_mul_f32 v[30:31], v[210:211], v[30:31] op_sel_hi:[0,1]
	v_pk_mul_f32 v[28:29], v[210:211], v[28:29] op_sel_hi:[0,1]
	v_pk_mul_f32 v[26:27], v[210:211], v[26:27] op_sel_hi:[0,1]
	v_pk_mul_f32 v[24:25], v[210:211], v[24:25] op_sel_hi:[0,1]
	v_pk_mul_f32 v[22:23], v[210:211], v[22:23] op_sel_hi:[0,1]
	v_pk_mul_f32 v[20:21], v[210:211], v[20:21] op_sel_hi:[0,1]
	v_pk_mul_f32 v[18:19], v[210:211], v[18:19] op_sel_hi:[0,1]
	v_pk_mul_f32 v[16:17], v[210:211], v[16:17] op_sel_hi:[0,1]
.Lgqa_slow_883:
	s_waitcnt lgkmcnt(0)
	s_barrier
	ds_read_b128 v[64:67], v216 offset:32768
	ds_read_b128 v[68:71], v216 offset:40960
	ds_read_b128 v[162:165], v218 offset:32768
	ds_read_b128 v[166:169], v218 offset:40960
	v_exp_f32_e32 v112, v112
	v_exp_f32_e32 v113, v113
	s_waitcnt lgkmcnt(3)
	v_mfma_f32_32x32x16_bf16 v[96:111], v[64:67], v[138:141], 0
	v_exp_f32_e32 v114, v114
	v_exp_f32_e32 v115, v115
	v_exp_f32_e32 v116, v116
	v_exp_f32_e32 v117, v117
	v_exp_f32_e32 v118, v118
	v_exp_f32_e32 v119, v119
	s_waitcnt lgkmcnt(2)
	v_mfma_f32_32x32x16_bf16 v[64:79], v[68:71], v[138:141], 0
	s_waitcnt lgkmcnt(1)
	v_mfma_f32_32x32x16_bf16 v[96:111], v[162:165], v[154:157], v[96:111]
	s_waitcnt lgkmcnt(0)
	v_mfma_f32_32x32x16_bf16 v[64:79], v[166:169], v[154:157], v[64:79]
	ds_read_b128 v[162:165], v219 offset:32768
	ds_read_b128 v[166:169], v219 offset:40960
	s_waitcnt lgkmcnt(1)
	v_mfma_f32_32x32x16_bf16 v[96:111], v[162:165], v[158:161], v[96:111]
	s_waitcnt lgkmcnt(0)
	v_mfma_f32_32x32x16_bf16 v[64:79], v[166:169], v[158:161], v[64:79]
	ds_read_b128 v[162:165], v220 offset:32768
	ds_read_b128 v[166:169], v220 offset:40960
	s_waitcnt lgkmcnt(1)
	v_mfma_f32_32x32x16_bf16 v[96:111], v[162:165], v[150:153], v[96:111]
	s_waitcnt lgkmcnt(0)
	v_mfma_f32_32x32x16_bf16 v[64:79], v[166:169], v[150:153], v[64:79]
	ds_read_b128 v[162:165], v221 offset:32768
	ds_read_b128 v[166:169], v221 offset:40960
	s_waitcnt lgkmcnt(1)
	v_mfma_f32_32x32x16_bf16 v[96:111], v[162:165], v[146:149], v[96:111]
	s_waitcnt lgkmcnt(0)
	v_mfma_f32_32x32x16_bf16 v[64:79], v[166:169], v[146:149], v[64:79]
	ds_read_b128 v[162:165], v222 offset:32768
	ds_read_b128 v[166:169], v222 offset:40960
	s_waitcnt lgkmcnt(1)
	v_mfma_f32_32x32x16_bf16 v[96:111], v[162:165], v[142:145], v[96:111]
	s_waitcnt lgkmcnt(0)
	v_mfma_f32_32x32x16_bf16 v[64:79], v[166:169], v[142:145], v[64:79]
	ds_read_b128 v[162:165], v224 offset:32768
	ds_read_b128 v[166:169], v224 offset:40960
	s_waitcnt lgkmcnt(1)
	v_mfma_f32_32x32x16_bf16 v[96:111], v[162:165], v[134:137], v[96:111]
	s_waitcnt lgkmcnt(0)
	v_mfma_f32_32x32x16_bf16 v[64:79], v[166:169], v[134:137], v[64:79]
	ds_read_b128 v[162:165], v223 offset:32768
	ds_read_b128 v[166:169], v223 offset:40960
	s_waitcnt lgkmcnt(1)
	v_mfma_f32_32x32x16_bf16 v[96:111], v[162:165], v[130:133], v[96:111]
	v_exp_f32_e32 v162, v120
	v_exp_f32_e32 v163, v121
	v_exp_f32_e32 v164, v122
	v_exp_f32_e32 v165, v123
	v_add_f32_e32 v120, v80, v81
	v_add_f32_e32 v121, v88, v89
	v_add_f32_e32 v122, v112, v113
	s_waitcnt lgkmcnt(0)
	v_mfma_f32_32x32x16_bf16 v[64:79], v[166:169], v[130:133], v[64:79]
	v_exp_f32_e32 v166, v124
	v_exp_f32_e32 v167, v125
	v_add_f32_e32 v123, v162, v163
	v_exp_f32_e32 v168, v126
	v_add_f32_e32 v120, v82, v120
	v_add_f32_e32 v121, v90, v121
	v_add_f32_e32 v122, v114, v122
	v_add_f32_e32 v123, v164, v123
	v_exp_f32_e32 v169, v127
	v_add_f32_e32 v120, v83, v120
	v_add_f32_e32 v121, v91, v121
	v_add_f32_e32 v122, v115, v122
	v_add_f32_e32 v123, v165, v123
	v_add_f32_e32 v120, v84, v120
	v_add_f32_e32 v121, v92, v121
	v_add_f32_e32 v122, v116, v122
	v_add_f32_e32 v123, v166, v123
	v_add_f32_e32 v120, v85, v120
	v_add_f32_e32 v121, v93, v121
	v_add_f32_e32 v122, v117, v122
	v_add_f32_e32 v123, v167, v123
	v_add_f32_e32 v120, v86, v120
	v_add_f32_e32 v121, v94, v121
	v_add_f32_e32 v122, v118, v122
	v_add_f32_e32 v123, v168, v123
	v_add_f32_e32 v120, v87, v120
	v_add_f32_e32 v121, v95, v121
	v_add_f32_e32 v122, v119, v122
	v_add_f32_e32 v123, v169, v123
	v_add_f32_e32 v120, v121, v120
	v_add_f32_e32 v121, v123, v122
	v_add_f32_e32 v229, v120, v121
	v_mov_b32_e32 v233, v229
	s_nop 1
	v_permlane32_swap_b32_e32 v229, v233
	v_cvt_pk_bf16_f32 v124, v80, v81
	v_cvt_pk_bf16_f32 v125, v82, v83
	v_cvt_pk_bf16_f32 v126, v84, v85
	v_cvt_pk_bf16_f32 v127, v86, v87
	v_cvt_pk_bf16_f32 v120, v88, v89
	v_cvt_pk_bf16_f32 v121, v90, v91
	v_cvt_pk_bf16_f32 v122, v92, v93
	v_cvt_pk_bf16_f32 v123, v94, v95
	v_cvt_pk_bf16_f32 v112, v112, v113
	v_cvt_pk_bf16_f32 v113, v114, v115
	v_cvt_pk_bf16_f32 v114, v116, v117
	v_cvt_pk_bf16_f32 v115, v118, v119
	v_cvt_pk_bf16_f32 v116, v162, v163
	v_cvt_pk_bf16_f32 v117, v164, v165
	v_cvt_pk_bf16_f32 v118, v166, v167
	v_cvt_pk_bf16_f32 v119, v168, v169
	s_min_i32 s2, s39, s14
	s_mul_i32 s2, s2, s62
	s_lshl_b32 s72, s2, 6
	s_lshl_b64 s[2:3], s[72:73], 1
	s_add_u32 s12, s10, s2
	s_addc_u32 s13, s11, s3
	s_add_u32 s2, s8, s2
	s_addc_u32 s3, s9, s3
	v_lshl_add_u64 v[80:81], s[12:13], 0, v[128:129]
	v_lshl_add_u64 v[82:83], s[12:13], 0, v[198:199]
	global_load_dwordx4 v[162:165], v[80:81], off
	global_load_dwordx4 v[166:169], v[82:83], off
	v_lshl_add_u64 v[80:81], s[2:3], 0, v[128:129]
	v_lshl_add_u64 v[82:83], s[2:3], 0, v[198:199]
	global_load_dwordx4 v[170:173], v[80:81], off
	global_load_dwordx4 v[174:177], v[82:83], off
	ds_read_b64_tr_b16 v[80:81], v211 offset:0
	ds_read_b64_tr_b16 v[82:83], v211 offset:0x800
	ds_read_b64_tr_b16 v[84:85], v211 offset:0x1000
	ds_read_b64_tr_b16 v[86:87], v211 offset:0x1800
	ds_read_b64_tr_b16 v[88:89], v211 offset:0x2000
	ds_read_b64_tr_b16 v[90:91], v211 offset:0x2800
	ds_read_b64_tr_b16 v[92:93], v211 offset:0x3000
	ds_read_b64_tr_b16 v[94:95], v211 offset:0x3800
	s_waitcnt lgkmcnt(0)
	s_nop 0
	v_mfma_f32_32x32x16_bf16 v[0:15], v[80:83], v[124:127], v[0:15]
	v_max_f32_e32 v80, v65, v65
	v_max_f32_e32 v81, v64, v64
	v_max_f32_e32 v80, v81, v80
	v_max3_f32 v81, v96, v97, v98
	v_max3_f32 v80, v80, v66, v67
	v_max3_f32 v81, v81, v99, v100
	v_max3_f32 v80, v80, v68, v69
	v_mfma_f32_32x32x16_bf16 v[0:15], v[84:87], v[120:123], v[0:15]
	v_max3_f32 v81, v81, v101, v102
	v_max3_f32 v80, v80, v70, v71
	v_max3_f32 v81, v81, v103, v104
	v_max3_f32 v80, v80, v72, v73
	v_max3_f32 v81, v81, v105, v106
	v_max3_f32 v80, v80, v74, v75
	v_max3_f32 v81, v81, v107, v108
	v_mfma_f32_32x32x16_bf16 v[0:15], v[88:91], v[112:115], v[0:15]
	v_max3_f32 v80, v80, v76, v77
	v_max3_f32 v81, v81, v109, v110
	v_max3_f32 v80, v80, v78, v79
	v_max3_f32 v194, v81, v111, v80
	ds_read_b64_tr_b16 v[80:81], v211 offset:0x200
	ds_read_b64_tr_b16 v[82:83], v211 offset:0xa00
	ds_read_b64_tr_b16 v[84:85], v211 offset:0x1200
	v_mfma_f32_32x32x16_bf16 v[0:15], v[92:95], v[116:119], v[0:15]
	ds_read_b64_tr_b16 v[86:87], v211 offset:0x1a00
	ds_read_b64_tr_b16 v[88:89], v211 offset:0x2200
	ds_read_b64_tr_b16 v[90:91], v211 offset:0x2a00
	ds_read_b64_tr_b16 v[92:93], v211 offset:0x3200
	ds_read_b64_tr_b16 v[94:95], v211 offset:0x3a00
	s_waitcnt lgkmcnt(0)
	v_mfma_f32_32x32x16_bf16 v[48:63], v[80:83], v[124:127], v[48:63]
	v_mov_b32_e32 v80, v194
	s_nop 1
	v_permlane32_swap_b32_e32 v194, v80
	v_max_f32_e32 v80, v80, v80
	v_max_f32_e32 v81, v194, v194
	v_max_f32_e32 v80, v81, v80
	v_sub_f32_e32 v81, v80, v226
	v_mfma_f32_32x32x16_bf16 v[48:63], v[84:87], v[120:123], v[48:63]
	v_cmp_ge_f32_e32 vcc, s31, v81
	v_max_f32_e32 v81, v226, v226
	v_max_f32_e32 v80, v81, v80
	v_sub_f32_e32 v81, v226, v80
	v_mul_f32_e32 v81, 0x3e0293ee, v81
	v_exp_f32_e32 v81, v81
	s_cmp_eq_u64 vcc, exec
	v_mfma_f32_32x32x16_bf16 v[48:63], v[88:91], v[112:115], v[48:63]
	s_cselect_b64 vcc, -1, 0
	v_cndmask_b32_e64 v208, v81, 1.0, vcc
	v_cndmask_b32_e32 v226, v80, v226, vcc
	ds_read_b64_tr_b16 v[80:81], v211 offset:0x400
	ds_read_b64_tr_b16 v[82:83], v211 offset:0xc00
	ds_read_b64_tr_b16 v[84:85], v211 offset:0x1400
	ds_read_b64_tr_b16 v[86:87], v211 offset:0x1c00
	v_mfma_f32_32x32x16_bf16 v[48:63], v[92:95], v[116:119], v[48:63]
	ds_read_b64_tr_b16 v[88:89], v211 offset:0x2400
	ds_read_b64_tr_b16 v[90:91], v211 offset:0x2c00
	ds_read_b64_tr_b16 v[92:93], v211 offset:0x3400
	ds_read_b64_tr_b16 v[94:95], v211 offset:0x3c00
	s_waitcnt lgkmcnt(0)
	v_mul_f32_e32 v234, 0xbe0293ee, v226
	v_fmamk_f32 v96, v96, 0x3e0293ee, v234
	v_fmamk_f32 v97, v97, 0x3e0293ee, v234
	v_fmamk_f32 v98, v98, 0x3e0293ee, v234
	v_fmamk_f32 v99, v99, 0x3e0293ee, v234
	v_fmamk_f32 v100, v100, 0x3e0293ee, v234
	v_fmamk_f32 v101, v101, 0x3e0293ee, v234
	v_fmamk_f32 v102, v102, 0x3e0293ee, v234
	v_fmamk_f32 v103, v103, 0x3e0293ee, v234
	v_fmamk_f32 v104, v104, 0x3e0293ee, v234
	v_fmamk_f32 v105, v105, 0x3e0293ee, v234
	v_fmamk_f32 v106, v106, 0x3e0293ee, v234
	v_fmamk_f32 v107, v107, 0x3e0293ee, v234
	v_fmamk_f32 v108, v108, 0x3e0293ee, v234
	v_fmamk_f32 v109, v109, 0x3e0293ee, v234
	v_fmamk_f32 v110, v110, 0x3e0293ee, v234
	v_fmamk_f32 v111, v111, 0x3e0293ee, v234
	v_mfma_f32_32x32x16_bf16 v[32:47], v[80:83], v[124:127], v[32:47]
	v_fma_f32 v80, v64, s52, v234
	v_fma_f32 v81, v65, s52, v234
	v_exp_f32_e32 v64, v96
	v_exp_f32_e32 v65, v97
	v_pk_fma_f32 v[82:83], v[66:67], s[52:53], v[234:235] op_sel_hi:[1,0,0]
	v_exp_f32_e32 v66, v98
	v_exp_f32_e32 v67, v99
	v_mfma_f32_32x32x16_bf16 v[32:47], v[84:87], v[120:123], v[32:47]
	v_fma_f32 v84, v68, s52, v234
	v_fma_f32 v85, v69, s52, v234
	v_exp_f32_e32 v68, v100
	v_exp_f32_e32 v69, v101
	v_pk_fma_f32 v[86:87], v[70:71], s[52:53], v[234:235] op_sel_hi:[1,0,0]
	v_exp_f32_e32 v70, v102
	v_exp_f32_e32 v71, v103
	v_mfma_f32_32x32x16_bf16 v[32:47], v[88:91], v[112:115], v[32:47]
	v_fma_f32 v88, v72, s52, v234
	v_fma_f32 v89, v73, s52, v234
	ds_read_b64_tr_b16 v[72:73], v211 offset:0x600
	v_fma_f32 v90, v74, s52, v234
	v_fma_f32 v91, v75, s52, v234
	ds_read_b64_tr_b16 v[74:75], v211 offset:0xe00
	v_mfma_f32_32x32x16_bf16 v[32:47], v[92:95], v[116:119], v[32:47]
	v_fma_f32 v92, v76, s52, v234
	v_fma_f32 v93, v77, s52, v234
	ds_read_b64_tr_b16 v[76:77], v211 offset:0x1600
	v_fma_f32 v94, v78, s52, v234
	v_fma_f32 v95, v79, s52, v234
	ds_read_b64_tr_b16 v[78:79], v211 offset:0x1e00
	ds_read_b64_tr_b16 v[96:97], v211 offset:0x2600
	ds_read_b64_tr_b16 v[98:99], v211 offset:0x2e00
	ds_read_b64_tr_b16 v[100:101], v211 offset:0x3600
	ds_read_b64_tr_b16 v[102:103], v211 offset:0x3e00
	s_waitcnt lgkmcnt(0)
	v_mfma_f32_32x32x16_bf16 v[16:31], v[72:75], v[124:127], v[16:31]
	v_exp_f32_e32 v72, v104
	v_exp_f32_e32 v73, v105
	v_exp_f32_e32 v74, v106
	v_exp_f32_e32 v75, v107
	v_cmp_gt_f32_e32 vcc, 1.0, v208
	v_mfma_f32_32x32x16_bf16 v[16:31], v[76:79], v[120:123], v[16:31]
	v_exp_f32_e32 v76, v108
	v_exp_f32_e32 v77, v109
	v_exp_f32_e32 v78, v110
	v_exp_f32_e32 v79, v111
	s_barrier
	v_mfma_f32_32x32x16_bf16 v[16:31], v[96:99], v[112:115], v[16:31]
	s_waitcnt vmcnt(4)
	s_waitcnt vmcnt(7)
	ds_write_b128 v212, v[178:181] offset:16384
	s_waitcnt vmcnt(6)
	ds_write_b128 v213, v[182:185] offset:16384
	s_waitcnt vmcnt(5)
	ds_write_b128 v214, v[186:189] offset:49152
	s_waitcnt vmcnt(4)
	ds_write_b128 v215, v[190:193] offset:49152
	v_mfma_f32_32x32x16_bf16 v[16:31], v[100:103], v[116:119], v[16:31]
	s_cbranch_vccz .Lgqa_slow_885
	v_pk_mul_f32 v[14:15], v[14:15], v[208:209] op_sel_hi:[1,0]
	v_pk_mul_f32 v[12:13], v[12:13], v[208:209] op_sel_hi:[1,0]
	v_pk_mul_f32 v[10:11], v[10:11], v[208:209] op_sel_hi:[1,0]
	v_pk_mul_f32 v[8:9], v[8:9], v[208:209] op_sel_hi:[1,0]
	v_pk_mul_f32 v[6:7], v[6:7], v[208:209] op_sel_hi:[1,0]
	v_pk_mul_f32 v[4:5], v[4:5], v[208:209] op_sel_hi:[1,0]
	v_pk_mul_f32 v[2:3], v[2:3], v[208:209] op_sel_hi:[1,0]
	v_pk_mul_f32 v[0:1], v[0:1], v[208:209] op_sel_hi:[1,0]
	v_pk_mul_f32 v[62:63], v[62:63], v[208:209] op_sel_hi:[1,0]
	v_pk_mul_f32 v[60:61], v[60:61], v[208:209] op_sel_hi:[1,0]
	v_pk_mul_f32 v[58:59], v[58:59], v[208:209] op_sel_hi:[1,0]
	v_pk_mul_f32 v[56:57], v[56:57], v[208:209] op_sel_hi:[1,0]
	v_pk_mul_f32 v[54:55], v[54:55], v[208:209] op_sel_hi:[1,0]
	v_pk_mul_f32 v[52:53], v[52:53], v[208:209] op_sel_hi:[1,0]
	v_pk_mul_f32 v[50:51], v[50:51], v[208:209] op_sel_hi:[1,0]
	v_pk_mul_f32 v[48:49], v[48:49], v[208:209] op_sel_hi:[1,0]
	v_pk_mul_f32 v[46:47], v[208:209], v[46:47] op_sel_hi:[0,1]
	v_pk_mul_f32 v[44:45], v[208:209], v[44:45] op_sel_hi:[0,1]
	v_pk_mul_f32 v[42:43], v[208:209], v[42:43] op_sel_hi:[0,1]
	v_pk_mul_f32 v[40:41], v[208:209], v[40:41] op_sel_hi:[0,1]
	v_pk_mul_f32 v[38:39], v[208:209], v[38:39] op_sel_hi:[0,1]
	v_pk_mul_f32 v[36:37], v[208:209], v[36:37] op_sel_hi:[0,1]
	v_pk_mul_f32 v[34:35], v[208:209], v[34:35] op_sel_hi:[0,1]
	v_pk_mul_f32 v[32:33], v[208:209], v[32:33] op_sel_hi:[0,1]
	v_pk_mul_f32 v[30:31], v[208:209], v[30:31] op_sel_hi:[0,1]
	v_pk_mul_f32 v[28:29], v[208:209], v[28:29] op_sel_hi:[0,1]
	v_pk_mul_f32 v[26:27], v[208:209], v[26:27] op_sel_hi:[0,1]
	v_pk_mul_f32 v[24:25], v[208:209], v[24:25] op_sel_hi:[0,1]
	v_pk_mul_f32 v[22:23], v[208:209], v[22:23] op_sel_hi:[0,1]
	v_pk_mul_f32 v[20:21], v[208:209], v[20:21] op_sel_hi:[0,1]
	v_pk_mul_f32 v[18:19], v[208:209], v[18:19] op_sel_hi:[0,1]
	v_pk_mul_f32 v[16:17], v[208:209], v[16:17] op_sel_hi:[0,1]

.Lgqa_slow_887:
	ds_read_b128 v[96:99], v216 offset:49152
	ds_read_b128 v[100:103], v216 offset:57344
	v_exp_f32_e32 v80, v80
	v_exp_f32_e32 v81, v81
	v_exp_f32_e32 v88, v88
	s_waitcnt lgkmcnt(1)
	v_mfma_f32_32x32x16_bf16 v[112:127], v[96:99], v[138:141], 0
	v_exp_f32_e32 v89, v89
	v_exp_f32_e32 v82, v82
	v_exp_f32_e32 v90, v90
	v_exp_f32_e32 v83, v83
	v_exp_f32_e32 v91, v91
	v_exp_f32_e32 v84, v84
	v_exp_f32_e32 v92, v92
	s_waitcnt lgkmcnt(0)
	v_mfma_f32_32x32x16_bf16 v[96:111], v[100:103], v[138:141], 0
	ds_read_b128 v[138:141], v218 offset:49152
	s_waitcnt vmcnt(3)
	ds_read_b128 v[162:165], v218 offset:57344
	v_exp_f32_e32 v85, v85
	v_exp_f32_e32 v93, v93
	v_add_f32_e32 v128, v64, v65
	v_exp_f32_e32 v86, v86
	v_exp_f32_e32 v94, v94
	v_add_f32_e32 v128, v66, v128
	s_waitcnt lgkmcnt(1)
	v_mfma_f32_32x32x16_bf16 v[112:127], v[138:141], v[154:157], v[112:127]
	v_exp_f32_e32 v87, v87
	v_exp_f32_e32 v95, v95
	v_add_f32_e32 v128, v67, v128
	v_add_f32_e32 v128, v68, v128
	v_add_f32_e32 v128, v69, v128
	v_add_f32_e32 v128, v70, v128
	v_add_f32_e32 v128, v71, v128
	s_waitcnt lgkmcnt(0)
	v_mfma_f32_32x32x16_bf16 v[96:111], v[162:165], v[154:157], v[96:111]
	ds_read_b128 v[138:141], v219 offset:49152
	ds_read_b128 v[154:157], v219 offset:57344
	s_waitcnt lgkmcnt(1)
	v_mfma_f32_32x32x16_bf16 v[112:127], v[138:141], v[158:161], v[112:127]
	s_waitcnt lgkmcnt(0)
	v_mfma_f32_32x32x16_bf16 v[96:111], v[154:157], v[158:161], v[96:111]
	ds_read_b128 v[138:141], v220 offset:49152
	ds_read_b128 v[154:157], v220 offset:57344
	s_waitcnt lgkmcnt(1)
	v_mfma_f32_32x32x16_bf16 v[112:127], v[138:141], v[150:153], v[112:127]
	s_waitcnt lgkmcnt(0)
	v_mfma_f32_32x32x16_bf16 v[96:111], v[154:157], v[150:153], v[96:111]
	ds_read_b128 v[138:141], v221 offset:49152
	ds_read_b128 v[150:153], v221 offset:57344
	s_waitcnt lgkmcnt(1)
	v_mfma_f32_32x32x16_bf16 v[112:127], v[138:141], v[146:149], v[112:127]
	s_waitcnt lgkmcnt(0)
	v_mfma_f32_32x32x16_bf16 v[96:111], v[150:153], v[146:149], v[96:111]
	ds_read_b128 v[138:141], v222 offset:49152
	ds_read_b128 v[146:149], v222 offset:57344
	s_waitcnt lgkmcnt(1)
	v_mfma_f32_32x32x16_bf16 v[112:127], v[138:141], v[142:145], v[112:127]
	s_waitcnt lgkmcnt(0)
	v_mfma_f32_32x32x16_bf16 v[96:111], v[146:149], v[142:145], v[96:111]
	ds_read_b128 v[138:141], v224 offset:49152
	ds_read_b128 v[142:145], v224 offset:57344
	s_waitcnt lgkmcnt(1)
	v_mfma_f32_32x32x16_bf16 v[112:127], v[138:141], v[134:137], v[112:127]
	s_waitcnt lgkmcnt(0)
	v_mfma_f32_32x32x16_bf16 v[96:111], v[142:145], v[134:137], v[96:111]
	ds_read_b128 v[134:137], v223 offset:49152
	ds_read_b128 v[138:141], v223 offset:57344
	s_waitcnt lgkmcnt(1)
	v_mfma_f32_32x32x16_bf16 v[112:127], v[134:137], v[130:133], v[112:127]
	s_waitcnt lgkmcnt(0)
	v_mfma_f32_32x32x16_bf16 v[96:111], v[138:141], v[130:133], v[96:111]
	v_add_f32_e32 v130, v72, v73
	v_add_f32_e32 v131, v80, v81
	v_add_f32_e32 v132, v88, v89
	v_add_f32_e32 v130, v74, v130
	v_add_f32_e32 v131, v82, v131
	v_add_f32_e32 v132, v90, v132
	v_add_f32_e32 v130, v75, v130
	v_add_f32_e32 v131, v83, v131
	v_add_f32_e32 v132, v91, v132
	v_add_f32_e32 v130, v76, v130
	v_add_f32_e32 v131, v84, v131
	v_add_f32_e32 v132, v92, v132
	v_add_f32_e32 v130, v77, v130
	v_add_f32_e32 v131, v85, v131
	v_add_f32_e32 v132, v93, v132
	v_add_f32_e32 v130, v78, v130
	v_add_f32_e32 v131, v86, v131
	v_add_f32_e32 v132, v94, v132
	v_add_f32_e32 v130, v79, v130
	v_add_f32_e32 v131, v87, v131
	v_add_f32_e32 v132, v95, v132
	v_add_f32_e32 v128, v130, v128
	v_add_f32_e32 v130, v132, v131
	v_add_f32_e32 v142, v128, v130
	v_mov_b32_e32 v143, v142
	v_cvt_pk_bf16_f32 v130, v64, v65
	v_cvt_pk_bf16_f32 v131, v66, v67
	v_cvt_pk_bf16_f32 v132, v68, v69
	v_cvt_pk_bf16_f32 v133, v70, v71
	v_cvt_pk_bf16_f32 v72, v72, v73
	v_cvt_pk_bf16_f32 v73, v74, v75
	v_cvt_pk_bf16_f32 v74, v76, v77
	v_cvt_pk_bf16_f32 v75, v78, v79
	s_nop 1
	v_permlane32_swap_b32_e32 v142, v143
	v_cvt_pk_bf16_f32 v138, v80, v81
	v_cvt_pk_bf16_f32 v139, v82, v83
	v_cvt_pk_bf16_f32 v140, v84, v85
	v_cvt_pk_bf16_f32 v141, v86, v87
	v_cvt_pk_bf16_f32 v134, v88, v89
	v_cvt_pk_bf16_f32 v135, v90, v91
	v_cvt_pk_bf16_f32 v136, v92, v93
	v_cvt_pk_bf16_f32 v137, v94, v95
	ds_read_b64_tr_b16 v[64:65], v209 offset:0
	ds_read_b64_tr_b16 v[66:67], v209 offset:0x800
	ds_read_b64_tr_b16 v[68:69], v209 offset:0x1000
	ds_read_b64_tr_b16 v[70:71], v209 offset:0x1800
	ds_read_b64_tr_b16 v[76:77], v209 offset:0x2000
	ds_read_b64_tr_b16 v[78:79], v209 offset:0x2800
	ds_read_b64_tr_b16 v[80:81], v209 offset:0x3000
	ds_read_b64_tr_b16 v[82:83], v209 offset:0x3800
	s_waitcnt lgkmcnt(0)
	s_nop 0
	v_mfma_f32_32x32x16_bf16 v[0:15], v[64:67], v[130:133], v[0:15]
	v_max_f32_e32 v64, v97, v97
	v_max_f32_e32 v65, v96, v96
	v_max_f32_e32 v64, v65, v64
	v_max3_f32 v65, v112, v113, v114
	v_max3_f32 v64, v64, v98, v99
	v_max3_f32 v65, v65, v115, v116
	v_max3_f32 v64, v64, v100, v101
	v_mfma_f32_32x32x16_bf16 v[0:15], v[68:71], v[72:75], v[0:15]
	v_max3_f32 v65, v65, v117, v118
	v_max3_f32 v64, v64, v102, v103
	v_max3_f32 v65, v65, v119, v120
	v_max3_f32 v64, v64, v104, v105
	v_max3_f32 v65, v65, v121, v122
	v_max3_f32 v64, v64, v106, v107
	v_max3_f32 v65, v65, v123, v124
	v_mfma_f32_32x32x16_bf16 v[0:15], v[76:79], v[138:141], v[0:15]
	v_max3_f32 v64, v64, v108, v109
	v_max3_f32 v65, v65, v125, v126
	v_max3_f32 v64, v64, v110, v111
	v_max3_f32 v84, v65, v127, v64
	ds_read_b64_tr_b16 v[64:65], v209 offset:0x200
	ds_read_b64_tr_b16 v[66:67], v209 offset:0xa00
	ds_read_b64_tr_b16 v[68:69], v209 offset:0x1200
	v_mfma_f32_32x32x16_bf16 v[0:15], v[80:83], v[134:137], v[0:15]
	ds_read_b64_tr_b16 v[70:71], v209 offset:0x1a00
	ds_read_b64_tr_b16 v[76:77], v209 offset:0x2200
	ds_read_b64_tr_b16 v[78:79], v209 offset:0x2a00
	ds_read_b64_tr_b16 v[80:81], v209 offset:0x3200
	ds_read_b64_tr_b16 v[82:83], v209 offset:0x3a00
	s_waitcnt lgkmcnt(0)
	v_mfma_f32_32x32x16_bf16 v[48:63], v[64:67], v[130:133], v[48:63]
	v_mov_b32_e32 v64, v84
	s_nop 1
	v_permlane32_swap_b32_e32 v84, v64
	v_max_f32_e32 v64, v64, v64
	v_max_f32_e32 v65, v84, v84
	v_max_f32_e32 v64, v65, v64
	v_sub_f32_e32 v65, v64, v226
	v_mfma_f32_32x32x16_bf16 v[48:63], v[68:71], v[72:75], v[48:63]
	v_cmp_ge_f32_e32 vcc, s31, v65
	v_max_f32_e32 v65, v226, v226
	v_max_f32_e32 v64, v65, v64
	v_sub_f32_e32 v65, v226, v64
	v_mul_f32_e32 v65, 0x3e0293ee, v65
	v_exp_f32_e32 v65, v65
	s_cmp_eq_u64 vcc, exec
	v_mfma_f32_32x32x16_bf16 v[48:63], v[76:79], v[138:141], v[48:63]
	s_cselect_b64 vcc, -1, 0
	v_cndmask_b32_e32 v64, v64, v226, vcc
	v_cndmask_b32_e64 v128, v65, 1.0, vcc
	v_mul_f32_e32 v144, 0xbe0293ee, v64
	ds_read_b64_tr_b16 v[64:65], v209 offset:0x400
	ds_read_b64_tr_b16 v[66:67], v209 offset:0xc00
	ds_read_b64_tr_b16 v[68:69], v209 offset:0x1400
	v_mfma_f32_32x32x16_bf16 v[48:63], v[80:83], v[134:137], v[48:63]
	ds_read_b64_tr_b16 v[70:71], v209 offset:0x1c00
	ds_read_b64_tr_b16 v[76:77], v209 offset:0x2400
	ds_read_b64_tr_b16 v[78:79], v209 offset:0x2c00
	ds_read_b64_tr_b16 v[80:81], v209 offset:0x3400
	ds_read_b64_tr_b16 v[82:83], v209 offset:0x3c00
	s_waitcnt lgkmcnt(0)
	v_fmamk_f32 v112, v112, 0x3e0293ee, v144
	v_fmamk_f32 v113, v113, 0x3e0293ee, v144
	v_fmamk_f32 v114, v114, 0x3e0293ee, v144
	v_fmamk_f32 v115, v115, 0x3e0293ee, v144
	v_fmamk_f32 v116, v116, 0x3e0293ee, v144
	v_fmamk_f32 v117, v117, 0x3e0293ee, v144
	v_fmamk_f32 v118, v118, 0x3e0293ee, v144
	v_fmamk_f32 v119, v119, 0x3e0293ee, v144
	v_fmamk_f32 v120, v120, 0x3e0293ee, v144
	v_fmamk_f32 v121, v121, 0x3e0293ee, v144
	v_fmamk_f32 v122, v122, 0x3e0293ee, v144
	v_fmamk_f32 v123, v123, 0x3e0293ee, v144
	v_fmamk_f32 v124, v124, 0x3e0293ee, v144
	v_fmamk_f32 v125, v125, 0x3e0293ee, v144
	v_fmamk_f32 v126, v126, 0x3e0293ee, v144
	v_fmamk_f32 v127, v127, 0x3e0293ee, v144
	v_mfma_f32_32x32x16_bf16 v[32:47], v[64:67], v[130:133], v[32:47]
	v_fma_f32 v84, v100, s52, v144
	v_fma_f32 v85, v101, s52, v144
	v_fma_f32 v86, v102, s52, v144
	v_fma_f32 v87, v103, s52, v144
	v_fma_f32 v88, v104, s52, v144
	v_fma_f32 v89, v105, s52, v144
	v_pk_fma_f32 v[90:91], v[106:107], s[52:53], v[144:145] op_sel_hi:[1,0,0]
	v_exp_f32_e32 v64, v112
	v_exp_f32_e32 v65, v113
	v_exp_f32_e32 v66, v114
	v_mfma_f32_32x32x16_bf16 v[32:47], v[68:71], v[72:75], v[32:47]
	v_exp_f32_e32 v67, v115
	v_exp_f32_e32 v68, v116
	v_exp_f32_e32 v69, v117
	v_exp_f32_e32 v70, v118
	v_exp_f32_e32 v71, v119
	v_pk_fma_f32 v[94:95], v[110:111], s[52:53], v[144:145] op_sel_hi:[1,0,0]
	v_pk_fma_f32 v[92:93], v[108:109], s[52:53], v[144:145] op_sel_hi:[1,0,0]
	v_mfma_f32_32x32x16_bf16 v[32:47], v[76:79], v[138:141], v[32:47]
	ds_read_b64_tr_b16 v[76:77], v209 offset:0x600
	ds_read_b64_tr_b16 v[78:79], v209 offset:0xe00
	v_mfma_f32_32x32x16_bf16 v[32:47], v[80:83], v[134:137], v[32:47]
	v_fma_f32 v80, v96, s52, v144
	v_fma_f32 v81, v97, s52, v144
	ds_read_b64_tr_b16 v[96:97], v209 offset:0x1600
	v_fma_f32 v82, v98, s52, v144
	v_fma_f32 v83, v99, s52, v144
	ds_read_b64_tr_b16 v[98:99], v209 offset:0x1e00
	ds_read_b64_tr_b16 v[100:101], v209 offset:0x2600
	ds_read_b64_tr_b16 v[102:103], v209 offset:0x2e00
	ds_read_b64_tr_b16 v[104:105], v209 offset:0x3600
	ds_read_b64_tr_b16 v[106:107], v209 offset:0x3e00
	s_waitcnt lgkmcnt(0)
	v_mfma_f32_32x32x16_bf16 v[16:31], v[76:79], v[130:133], v[16:31]
	v_exp_f32_e32 v76, v124
	v_exp_f32_e32 v77, v125
	v_exp_f32_e32 v78, v126
	v_exp_f32_e32 v79, v127
	v_cmp_gt_f32_e32 vcc, 1.0, v128
	v_mfma_f32_32x32x16_bf16 v[16:31], v[96:99], v[72:75], v[16:31]
	v_exp_f32_e32 v72, v120
	v_exp_f32_e32 v73, v121
	v_exp_f32_e32 v74, v122
	v_exp_f32_e32 v75, v123
	s_barrier
	v_mfma_f32_32x32x16_bf16 v[16:31], v[100:103], v[138:141], v[16:31]
	v_mfma_f32_32x32x16_bf16 v[16:31], v[104:107], v[134:137], v[16:31]
	s_cbranch_vccz .Lgqa_slow_873
	v_pk_mul_f32 v[14:15], v[14:15], v[128:129] op_sel_hi:[1,0]
	v_pk_mul_f32 v[12:13], v[12:13], v[128:129] op_sel_hi:[1,0]
	v_pk_mul_f32 v[10:11], v[10:11], v[128:129] op_sel_hi:[1,0]
	v_pk_mul_f32 v[8:9], v[8:9], v[128:129] op_sel_hi:[1,0]
	v_pk_mul_f32 v[6:7], v[6:7], v[128:129] op_sel_hi:[1,0]
	v_pk_mul_f32 v[4:5], v[4:5], v[128:129] op_sel_hi:[1,0]
	v_pk_mul_f32 v[2:3], v[2:3], v[128:129] op_sel_hi:[1,0]
	v_pk_mul_f32 v[0:1], v[0:1], v[128:129] op_sel_hi:[1,0]
	v_pk_mul_f32 v[62:63], v[62:63], v[128:129] op_sel_hi:[1,0]
	v_pk_mul_f32 v[60:61], v[60:61], v[128:129] op_sel_hi:[1,0]
	v_pk_mul_f32 v[58:59], v[58:59], v[128:129] op_sel_hi:[1,0]
	v_pk_mul_f32 v[56:57], v[56:57], v[128:129] op_sel_hi:[1,0]
	v_pk_mul_f32 v[54:55], v[54:55], v[128:129] op_sel_hi:[1,0]
	v_pk_mul_f32 v[52:53], v[52:53], v[128:129] op_sel_hi:[1,0]
	v_pk_mul_f32 v[50:51], v[50:51], v[128:129] op_sel_hi:[1,0]
	v_pk_mul_f32 v[48:49], v[48:49], v[128:129] op_sel_hi:[1,0]
	v_pk_mul_f32 v[46:47], v[128:129], v[46:47] op_sel_hi:[0,1]
	v_pk_mul_f32 v[44:45], v[128:129], v[44:45] op_sel_hi:[0,1]
	v_pk_mul_f32 v[42:43], v[128:129], v[42:43] op_sel_hi:[0,1]
	v_pk_mul_f32 v[40:41], v[128:129], v[40:41] op_sel_hi:[0,1]
	v_pk_mul_f32 v[38:39], v[128:129], v[38:39] op_sel_hi:[0,1]
	v_pk_mul_f32 v[36:37], v[128:129], v[36:37] op_sel_hi:[0,1]
	v_pk_mul_f32 v[34:35], v[128:129], v[34:35] op_sel_hi:[0,1]
	v_pk_mul_f32 v[32:33], v[128:129], v[32:33] op_sel_hi:[0,1]
	v_pk_mul_f32 v[30:31], v[128:129], v[30:31] op_sel_hi:[0,1]
	v_pk_mul_f32 v[28:29], v[128:129], v[28:29] op_sel_hi:[0,1]
	v_pk_mul_f32 v[26:27], v[128:129], v[26:27] op_sel_hi:[0,1]
	v_pk_mul_f32 v[24:25], v[128:129], v[24:25] op_sel_hi:[0,1]
	v_pk_mul_f32 v[22:23], v[128:129], v[22:23] op_sel_hi:[0,1]
	v_pk_mul_f32 v[20:21], v[128:129], v[20:21] op_sel_hi:[0,1]
	v_pk_mul_f32 v[18:19], v[128:129], v[18:19] op_sel_hi:[0,1]
	v_pk_mul_f32 v[16:17], v[128:129], v[16:17] op_sel_hi:[0,1]
	s_branch .Lgqa_slow_873
